# s22
# baseline (speedup 1.0000x reference)
.LBB1_5:
	v_lshlrev_b32_e32 v67, 4, v1
	v_lshrrev_b32_e32 v1, 1, v1
	v_lshrrev_b32_e32 v69, 5, v132
	v_ashrrev_i32_e32 v66, 4, v132
	v_bitop3_b32 v1, v1, v69, 7 bitop3:0x78
	s_add_u32 s22, s24, s2
	v_lshlrev_b32_e32 v68, 7, v66
	v_lshlrev_b32_e32 v1, 4, v1
	v_and_b32_e32 v0, 8, v0
	s_addc_u32 s90, s25, s3
	v_lshl_or_b32 v201, v66, 12, v67
	v_or3_b32 v0, v68, v1, v0
	v_add_u32_e32 v100, 0x10000, v0
	v_cvt_pk_f16_f32 v1, v64, v65
	v_cvt_pk_f16_f32 v0, v62, v63
	v_cvt_pk_f16_f32 v61, v60, v61
	v_cvt_pk_f16_f32 v60, v58, v59
	ds_write2st64_b64 v100, v[0:1], v[60:61] offset1:8
	v_cvt_pk_f16_f32 v1, v56, v57
	v_cvt_pk_f16_f32 v0, v54, v55
	v_cvt_pk_f16_f32 v53, v52, v53
	v_cvt_pk_f16_f32 v52, v50, v51
	ds_write2st64_b64 v100, v[0:1], v[52:53] offset0:16 offset1:24
	v_cvt_pk_f16_f32 v1, v48, v49
	v_cvt_pk_f16_f32 v0, v46, v47
	v_cvt_pk_f16_f32 v45, v44, v45
	v_cvt_pk_f16_f32 v44, v42, v43
	ds_write2st64_b64 v100, v[0:1], v[44:45] offset0:32 offset1:40
	v_cvt_pk_f16_f32 v1, v40, v41
	v_cvt_pk_f16_f32 v0, v38, v39
	v_cvt_pk_f16_f32 v37, v36, v37
	v_cvt_pk_f16_f32 v36, v34, v35
	ds_write2st64_b64 v100, v[0:1], v[36:37] offset0:48 offset1:56
	s_add_u32 s0, s22, 0x200
	s_addc_u32 s1, s90, 0
	s_add_u32 s70, s0, 0x20000
	s_addc_u32 s71, s1, 0
	s_add_u32 s72, s0, 0x40000
	s_addc_u32 s73, s1, 0
	s_add_u32 s92, s0, 0x60000
	s_addc_u32 s93, s1, 0
	s_add_u32 s94, s0, 0x80000
	s_addc_u32 s95, s1, 0
	s_add_u32 s96, s0, 0xa0000
	s_addc_u32 s97, s1, 0
	s_add_u32 s98, s0, 0xc0000
	s_addc_u32 s99, s1, 0
	s_add_u32 s80, s0, 0xe0000
	s_addc_u32 s81, s1, 0
	global_load_dwordx4 v[70:73], v201, s[0:1] nt
	global_load_dwordx4 v[42:45], v201, s[70:71] nt
	global_load_dwordx4 v[46:49], v201, s[72:73] nt
	global_load_dwordx4 v[66:69], v201, s[92:93] nt
	global_load_dwordx4 v[62:65], v201, s[94:95] nt
	global_load_dwordx4 v[58:61], v201, s[96:97] nt
	global_load_dwordx4 v[54:57], v201, s[98:99] nt
	global_load_dwordx4 v[50:53], v201, s[80:81] nt
	s_waitcnt vmcnt(8)
	s_waitcnt lgkmcnt(0)
	s_barrier
	ds_read_b128 v[34:37], v131
	ds_read_b128 v[38:41], v131 offset:2048
	ds_read_b128 v[74:77], v131 offset:4096
	ds_read_b128 v[78:81], v131 offset:6144
	ds_read_b128 v[82:85], v129
	ds_read_b128 v[86:89], v129 offset:2048
	s_add_u32 s70, s22, 0x300
	v_add_u32_e32 v95, 0x8000, v94
	v_lshl_add_u64 v[0:1], s[26:27], 0, v[196:197]
	s_addc_u32 s71, s90, 0
	v_readfirstlane_b32 s0, v95
	v_cvt_pk_f16_f32 v33, v32, v33
	s_cmp_lg_u32 s2, 0
	s_cbranch_scc1 .Lres_skip_0
	s_add_u32 m0, s0, 0x18000
	s_nop 0
	global_load_lds_dwordx4 v[0:1], off
.Lres_skip_0:
	v_cvt_pk_f16_f32 v32, v30, v31
	ds_write_b64 v100, v[32:33] offset:32768
	global_load_dwordx4 v[30:33], v201, s[70:71] nt
	s_setprio 1
	s_waitcnt lgkmcnt(1)
	v_mfma_f32_16x16x32_f16 v[90:93], v[82:85], v[34:37], 0
	v_mfma_f32_16x16x32_f16 v[102:105], v[82:85], v[38:41], 0
	v_mfma_f32_16x16x32_f16 v[106:109], v[82:85], v[74:77], 0
	v_mfma_f32_16x16x32_f16 v[82:85], v[82:85], v[78:81], 0
	v_mfma_f32_16x16x32_f16 v[110:113], v[86:89], v[34:37], 0
	v_mfma_f32_16x16x32_f16 v[114:117], v[86:89], v[38:41], 0
	v_mfma_f32_16x16x32_f16 v[118:121], v[86:89], v[74:77], 0
	v_mfma_f32_16x16x32_f16 v[86:89], v[86:89], v[78:81], 0
	s_setprio 0
	ds_read_b128 v[122:125], v129 offset:4096
	ds_read_b128 v[134:137], v129 offset:6144
	v_add_u32_e32 v96, 0xa000, v94
	v_lshl_add_u64 v[98:99], v[0:1], 0, s[58:59]
	v_readfirstlane_b32 s1, v96
	v_cvt_pk_f16_f32 v29, v28, v29
	s_cmp_lg_u32 s2, 0
	s_cbranch_scc1 .Lres_skip_1
	s_add_u32 m0, s1, 0x18000
	s_nop 0
	global_load_lds_dwordx4 v[98:99], off
.Lres_skip_1:
	v_cvt_pk_f16_f32 v28, v26, v27
	ds_write_b64 v100, v[28:29] offset:36864
	s_add_u32 s70, s22, 0x20300
	s_addc_u32 s71, s90, 0
	global_load_dwordx4 v[26:29], v201, s[70:71] nt
	s_setprio 1
	s_waitcnt lgkmcnt(1)
	v_mfma_f32_16x16x32_f16 v[138:141], v[122:125], v[34:37], 0
	v_mfma_f32_16x16x32_f16 v[142:145], v[122:125], v[38:41], 0
	v_mfma_f32_16x16x32_f16 v[146:149], v[122:125], v[74:77], 0
	v_mfma_f32_16x16x32_f16 v[122:125], v[122:125], v[78:81], 0
	v_mfma_f32_16x16x32_f16 v[150:153], v[134:137], v[34:37], 0
	v_mfma_f32_16x16x32_f16 v[154:157], v[134:137], v[38:41], 0
	v_mfma_f32_16x16x32_f16 v[158:161], v[134:137], v[74:77], 0
	v_mfma_f32_16x16x32_f16 v[134:137], v[134:137], v[78:81], 0
	s_setprio 0
	ds_read_b128 v[162:165], v129 offset:8192
	ds_read_b128 v[166:169], v129 offset:10240
	v_add_u32_e32 v97, 0xc000, v94
	v_lshl_add_u64 v[98:99], v[0:1], 0, s[60:61]
	v_readfirstlane_b32 s71, v97
	v_cvt_pk_f16_f32 v25, v24, v25
	s_cmp_lg_u32 s2, 0
	s_cbranch_scc1 .Lres_skip_2
	s_add_u32 m0, s71, 0x18000
	s_nop 0
	global_load_lds_dwordx4 v[98:99], off
.Lres_skip_2:
	v_cvt_pk_f16_f32 v24, v22, v23
	ds_write_b64 v100, v[24:25] offset:40960
	s_add_u32 s72, s22, 0x40300
	s_addc_u32 s73, s90, 0
	global_load_dwordx4 v[22:25], v201, s[72:73] nt
	s_setprio 1
	s_waitcnt lgkmcnt(1)
	v_mfma_f32_16x16x32_f16 v[170:173], v[162:165], v[34:37], 0
	v_mfma_f32_16x16x32_f16 v[174:177], v[162:165], v[38:41], 0
	v_mfma_f32_16x16x32_f16 v[178:181], v[162:165], v[74:77], 0
	v_mfma_f32_16x16x32_f16 v[162:165], v[162:165], v[78:81], 0
	v_mfma_f32_16x16x32_f16 v[182:185], v[166:169], v[34:37], 0
	v_mfma_f32_16x16x32_f16 v[186:189], v[166:169], v[38:41], 0
	v_mfma_f32_16x16x32_f16 v[190:193], v[166:169], v[74:77], 0
	v_mfma_f32_16x16x32_f16 v[166:169], v[166:169], v[78:81], 0
	s_setprio 0
	ds_read_b128 v[202:205], v129 offset:12288
	ds_read_b128 v[206:209], v129 offset:14336
	v_add_u32_e32 v98, 0xe000, v94
	v_lshl_add_u64 v[0:1], v[0:1], 0, s[62:63]
	v_readfirstlane_b32 s72, v98
	s_cmp_lg_u32 s2, 0
	s_cbranch_scc1 .Lres_skip_3
	s_add_u32 m0, s72, 0x18000
	s_nop 0
	s_nop 0
	global_load_lds_dwordx4 v[0:1], off
.Lres_skip_3:
	v_cvt_pk_f16_f32 v1, v20, v21
	v_cvt_pk_f16_f32 v0, v18, v19
	ds_write_b64 v100, v[0:1] offset:45056
	s_add_u32 s80, s22, 0x60300
	s_addc_u32 s81, s90, 0
	global_load_dwordx4 v[18:21], v201, s[80:81] nt
	s_setprio 1
	s_waitcnt lgkmcnt(1)
	v_mfma_f32_16x16x32_f16 v[210:213], v[202:205], v[34:37], 0
	v_mfma_f32_16x16x32_f16 v[214:217], v[202:205], v[38:41], 0
	v_mfma_f32_16x16x32_f16 v[218:221], v[202:205], v[74:77], 0
	v_mfma_f32_16x16x32_f16 v[202:205], v[202:205], v[78:81], 0
	v_mfma_f32_16x16x32_f16 v[74:77], v[206:209], v[74:77], 0
	v_mfma_f32_16x16x32_f16 v[78:81], v[206:209], v[78:81], 0
	v_mfma_f32_16x16x32_f16 v[222:225], v[206:209], v[34:37], 0
	v_mfma_f32_16x16x32_f16 v[226:229], v[206:209], v[38:41], 0
	s_setprio 0
	ds_read_b128 v[206:209], v128
	ds_read_b128 v[230:233], v128 offset:2048
	ds_read_b128 v[234:237], v128 offset:4096
	ds_read_b128 v[238:241], v128 offset:6144
	ds_read_b128 v[34:37], v130
	ds_read_b128 v[38:41], v130 offset:2048
	v_cvt_pk_f16_f32 v1, v16, v17
	v_cvt_pk_f16_f32 v0, v14, v15
	ds_write_b64 v100, v[0:1] offset:49152
	s_add_u32 s80, s22, 0x80300
	s_addc_u32 s81, s90, 0
	global_load_dwordx4 v[14:17], v201, s[80:81] nt
	s_setprio 1
	s_waitcnt lgkmcnt(1)
	v_mfma_f32_16x16x32_f16 v[90:93], v[34:37], v[206:209], v[90:93]
	v_mfma_f32_16x16x32_f16 v[102:105], v[34:37], v[230:233], v[102:105]
	v_mfma_f32_16x16x32_f16 v[106:109], v[34:37], v[234:237], v[106:109]
	v_mfma_f32_16x16x32_f16 v[82:85], v[34:37], v[238:241], v[82:85]
	v_mfma_f32_16x16x32_f16 v[110:113], v[38:41], v[206:209], v[110:113]
	v_mfma_f32_16x16x32_f16 v[114:117], v[38:41], v[230:233], v[114:117]
	v_mfma_f32_16x16x32_f16 v[118:121], v[38:41], v[234:237], v[118:121]
	v_mfma_f32_16x16x32_f16 v[86:89], v[38:41], v[238:241], v[86:89]
	s_setprio 0
	ds_read_b128 v[34:37], v130 offset:4096
	ds_read_b128 v[38:41], v130 offset:6144
	v_cvt_pk_f16_f32 v1, v12, v13
	v_cvt_pk_f16_f32 v0, v10, v11
	ds_write_b64 v100, v[0:1] offset:53248
	s_add_u32 s80, s22, 0xa0300
	s_addc_u32 s81, s90, 0
	global_load_dwordx4 v[10:13], v201, s[80:81] nt
	s_setprio 1
	s_waitcnt lgkmcnt(1)
	v_mfma_f32_16x16x32_f16 v[146:149], v[34:37], v[234:237], v[146:149]
	v_mfma_f32_16x16x32_f16 v[122:125], v[34:37], v[238:241], v[122:125]
	v_mfma_f32_16x16x32_f16 v[134:137], v[38:41], v[238:241], v[134:137]
	v_mfma_f32_16x16x32_f16 v[138:141], v[34:37], v[206:209], v[138:141]
	v_mfma_f32_16x16x32_f16 v[142:145], v[34:37], v[230:233], v[142:145]
	v_mfma_f32_16x16x32_f16 v[150:153], v[38:41], v[206:209], v[150:153]
	v_mfma_f32_16x16x32_f16 v[154:157], v[38:41], v[230:233], v[154:157]
	v_mfma_f32_16x16x32_f16 v[158:161], v[38:41], v[234:237], v[158:161]
	s_setprio 0
	ds_read_b128 v[38:41], v130 offset:8192
	ds_read_b128 v[242:245], v130 offset:10240
	v_cvt_pk_f16_f32 v1, v8, v9
	v_cvt_pk_f16_f32 v0, v6, v7
	ds_write_b64 v100, v[0:1] offset:57344
	s_add_u32 s80, s22, 0xc0300
	s_addc_u32 s81, s90, 0
	global_load_dwordx4 v[34:37], v201, s[80:81] nt
	s_setprio 1
	s_waitcnt lgkmcnt(1)
	v_mfma_f32_16x16x32_f16 v[6:9], v[38:41], v[206:209], v[170:173]
	v_mfma_f32_16x16x32_f16 v[170:173], v[38:41], v[230:233], v[174:177]
	v_mfma_f32_16x16x32_f16 v[174:177], v[38:41], v[234:237], v[178:181]
	v_mfma_f32_16x16x32_f16 v[162:165], v[38:41], v[238:241], v[162:165]
	v_mfma_f32_16x16x32_f16 v[178:181], v[242:245], v[206:209], v[182:185]
	v_mfma_f32_16x16x32_f16 v[182:185], v[242:245], v[230:233], v[186:189]
	v_mfma_f32_16x16x32_f16 v[186:189], v[242:245], v[234:237], v[190:193]
	v_mfma_f32_16x16x32_f16 v[166:169], v[242:245], v[238:241], v[166:169]
	s_setprio 0
	s_nop 0
	ds_read_b128 v[190:193], v130 offset:12288
	ds_read_b128 v[242:245], v130 offset:14336
	v_cvt_pk_f16_f32 v1, v4, v5
	v_cvt_pk_f16_f32 v0, v2, v3
	ds_write_b64 v100, v[0:1] offset:61440
	s_add_u32 s80, s22, 0xe0300
	s_addc_u32 s81, s90, 0
	global_load_dwordx4 v[38:41], v201, s[80:81] nt
	s_setprio 1
	s_waitcnt lgkmcnt(1)
	v_mfma_f32_16x16x32_f16 v[78:81], v[242:245], v[238:241], v[78:81]
	v_mfma_f32_16x16x32_f16 v[210:213], v[190:193], v[206:209], v[210:213]
	v_mfma_f32_16x16x32_f16 v[214:217], v[190:193], v[230:233], v[214:217]
	v_mfma_f32_16x16x32_f16 v[218:221], v[190:193], v[234:237], v[218:221]
	v_mfma_f32_16x16x32_f16 v[190:193], v[190:193], v[238:241], v[202:205]
	v_mfma_f32_16x16x32_f16 v[202:205], v[242:245], v[206:209], v[222:225]
	v_mfma_f32_16x16x32_f16 v[206:209], v[242:245], v[230:233], v[226:229]
	v_mfma_f32_16x16x32_f16 v[222:225], v[242:245], v[234:237], v[74:77]
	s_setprio 0
	s_waitcnt vmcnt(4)
	s_waitcnt lgkmcnt(0)
	s_barrier
	v_add_u32_e32 v250, 0x20000, v129
	v_add_u32_e32 v251, 0x20000, v130
	ds_read_b128 v[226:229], v131 offset:32768
	ds_read_b128 v[230:233], v131 offset:34816
	ds_read_b128 v[234:237], v131 offset:36864
	ds_read_b128 v[238:241], v131 offset:38912
	ds_read_b128 v[74:77], v250
	ds_read_b128 v[242:245], v250 offset:2048
	s_add_u32 s80, s22, 0x400
	s_addc_u32 s81, s90, 0
	v_lshl_add_u64 v[198:199], s[28:29], 0, v[196:197]
	v_readfirstlane_b32 s70, v94
	s_mov_b32 m0, s70
	v_cvt_pk_f16_f32 v1, v72, v73
	global_load_lds_dwordx4 v[198:199], off
	v_cvt_pk_f16_f32 v0, v70, v71
	ds_write_b64 v100, v[0:1]
	global_load_dwordx4 v[0:3], v201, s[80:81] nt
	s_setprio 1
	s_waitcnt lgkmcnt(1)
	v_mfma_f32_16x16x32_f16 v[70:73], v[74:77], v[226:229], v[90:93]
	v_mfma_f32_16x16x32_f16 v[90:93], v[74:77], v[230:233], v[102:105]
	v_mfma_f32_16x16x32_f16 v[104:107], v[74:77], v[234:237], v[106:109]
	v_mfma_f32_16x16x32_f16 v[82:85], v[74:77], v[238:241], v[82:85]
	v_mfma_f32_16x16x32_f16 v[108:111], v[242:245], v[226:229], v[110:113]
	v_mfma_f32_16x16x32_f16 v[112:115], v[242:245], v[230:233], v[114:117]
	v_mfma_f32_16x16x32_f16 v[116:119], v[242:245], v[234:237], v[118:121]
	v_mfma_f32_16x16x32_f16 v[86:89], v[242:245], v[238:241], v[86:89]
	s_setprio 0
	ds_read_b128 v[74:77], v250 offset:4096
	ds_read_b128 v[242:245], v250 offset:6144
	v_add_u32_e32 v99, 0x2000, v94
	v_lshl_add_u64 v[4:5], v[198:199], 0, s[58:59]
	v_readfirstlane_b32 s73, v99
	s_mov_b32 m0, s73
	s_nop 0
	global_load_lds_dwordx4 v[4:5], off
	v_cvt_pk_f16_f32 v5, v44, v45
	v_cvt_pk_f16_f32 v4, v42, v43
	ds_write_b64 v100, v[4:5] offset:4096
	s_add_u32 s80, s22, 0x20400
	s_addc_u32 s81, s90, 0
	global_load_dwordx4 v[42:45], v201, s[80:81] nt
	s_setprio 1
	s_waitcnt lgkmcnt(1)
	v_mfma_f32_16x16x32_f16 v[146:149], v[74:77], v[234:237], v[146:149]
	v_mfma_f32_16x16x32_f16 v[120:123], v[74:77], v[238:241], v[122:125]
	v_mfma_f32_16x16x32_f16 v[124:127], v[242:245], v[226:229], v[150:153]
	v_mfma_f32_16x16x32_f16 v[134:137], v[242:245], v[238:241], v[134:137]
	v_mfma_f32_16x16x32_f16 v[138:141], v[74:77], v[226:229], v[138:141]
	v_mfma_f32_16x16x32_f16 v[142:145], v[74:77], v[230:233], v[142:145]
	v_mfma_f32_16x16x32_f16 v[150:153], v[242:245], v[230:233], v[154:157]
	v_mfma_f32_16x16x32_f16 v[154:157], v[242:245], v[234:237], v[158:161]
	s_setprio 0
	ds_read_b128 v[74:77], v250 offset:8192
	s_nop 0
	ds_read_b128 v[158:161], v250 offset:10240
	v_add_u32_e32 v101, 0x4000, v94
	v_lshl_add_u64 v[4:5], v[198:199], 0, s[60:61]
	v_readfirstlane_b32 s91, v101
	s_mov_b32 m0, s91
	s_nop 0
	global_load_lds_dwordx4 v[4:5], off
	v_cvt_pk_f16_f32 v5, v48, v49
	v_cvt_pk_f16_f32 v4, v46, v47
	ds_write_b64 v100, v[4:5] offset:8192
	s_add_u32 s80, s22, 0x40400
	s_addc_u32 s81, s90, 0
	global_load_dwordx4 v[46:49], v201, s[80:81] nt
	s_setprio 1
	s_waitcnt lgkmcnt(1)
	v_mfma_f32_16x16x32_f16 v[4:7], v[74:77], v[226:229], v[6:9]
	v_mfma_f32_16x16x32_f16 v[170:173], v[74:77], v[230:233], v[170:173]
	v_mfma_f32_16x16x32_f16 v[174:177], v[74:77], v[234:237], v[174:177]
	v_mfma_f32_16x16x32_f16 v[162:165], v[74:77], v[238:241], v[162:165]
	v_mfma_f32_16x16x32_f16 v[178:181], v[158:161], v[226:229], v[178:181]
	v_mfma_f32_16x16x32_f16 v[182:185], v[158:161], v[230:233], v[182:185]
	v_mfma_f32_16x16x32_f16 v[186:189], v[158:161], v[234:237], v[186:189]
	v_mfma_f32_16x16x32_f16 v[158:161], v[158:161], v[238:241], v[166:169]
	s_setprio 0
	s_nop 1
	ds_read_b128 v[166:169], v250 offset:12288
	ds_read_b128 v[242:245], v250 offset:14336
	v_add_u32_e32 v102, 0x6000, v94
	v_lshl_add_u64 v[8:9], v[198:199], 0, s[62:63]
	v_readfirstlane_b32 s92, v102
	s_mov_b32 m0, s92
	s_nop 0
	global_load_lds_dwordx4 v[8:9], off
	v_cvt_pk_f16_f32 v9, v68, v69
	v_cvt_pk_f16_f32 v8, v66, v67
	ds_write_b64 v100, v[8:9] offset:12288
	s_add_u32 s80, s22, 0x60400
	s_addc_u32 s81, s90, 0
	global_load_dwordx4 v[74:77], v201, s[80:81] nt
	s_setprio 1
	s_waitcnt lgkmcnt(1)
	v_mfma_f32_16x16x32_f16 v[66:69], v[166:169], v[226:229], v[210:213]
	v_mfma_f32_16x16x32_f16 v[210:213], v[166:169], v[230:233], v[214:217]
	v_mfma_f32_16x16x32_f16 v[214:217], v[166:169], v[234:237], v[218:221]
	v_mfma_f32_16x16x32_f16 v[166:169], v[166:169], v[238:241], v[190:193]
	v_mfma_f32_16x16x32_f16 v[190:193], v[242:245], v[226:229], v[202:205]
	v_mfma_f32_16x16x32_f16 v[202:205], v[242:245], v[230:233], v[206:209]
	v_mfma_f32_16x16x32_f16 v[206:209], v[242:245], v[234:237], v[222:225]
	v_mfma_f32_16x16x32_f16 v[218:221], v[242:245], v[238:241], v[78:81]
	s_setprio 0
	s_nop 0
	ds_read_b128 v[222:225], v128 offset:32768
	ds_read_b128 v[226:229], v128 offset:34816
	ds_read_b128 v[230:233], v128 offset:36864
	ds_read_b128 v[234:237], v128 offset:38912
	ds_read_b128 v[238:241], v251
	ds_read_b128 v[242:245], v251 offset:2048
	v_cvt_pk_f16_f32 v9, v64, v65
	v_cvt_pk_f16_f32 v8, v62, v63
	ds_write_b64 v100, v[8:9] offset:16384
	s_add_u32 s80, s22, 0x80400
	s_addc_u32 s81, s90, 0
	global_load_dwordx4 v[78:81], v201, s[80:81] nt
	s_setprio 1
	s_waitcnt lgkmcnt(1)
	v_mfma_f32_16x16x32_f16 v[62:65], v[238:241], v[222:225], v[70:73]
	v_mfma_f32_16x16x32_f16 v[70:73], v[238:241], v[226:229], v[90:93]
	v_mfma_f32_16x16x32_f16 v[104:107], v[238:241], v[230:233], v[104:107]
	v_mfma_f32_16x16x32_f16 v[108:111], v[242:245], v[222:225], v[108:111]
	v_mfma_f32_16x16x32_f16 v[112:115], v[242:245], v[226:229], v[112:115]
	v_mfma_f32_16x16x32_f16 v[116:119], v[242:245], v[230:233], v[116:119]
	v_mfma_f32_16x16x32_f16 v[238:241], v[238:241], v[234:237], v[82:85]
	v_mfma_f32_16x16x32_f16 v[242:245], v[242:245], v[234:237], v[86:89]
	s_setprio 0
	s_nop 1
	ds_read_b128 v[86:89], v251 offset:4096
	ds_read_b128 v[90:93], v251 offset:6144
	v_cvt_pk_f16_f32 v9, v60, v61
	v_cvt_pk_f16_f32 v8, v58, v59
	ds_write_b64 v100, v[8:9] offset:20480
	s_add_u32 s80, s22, 0xa0400
	s_addc_u32 s81, s90, 0
	global_load_dwordx4 v[82:85], v201, s[80:81] nt
	s_setprio 1
	s_waitcnt lgkmcnt(1)
	v_mfma_f32_16x16x32_f16 v[58:61], v[86:89], v[222:225], v[138:141]
	v_mfma_f32_16x16x32_f16 v[138:141], v[86:89], v[226:229], v[142:145]
	v_mfma_f32_16x16x32_f16 v[142:145], v[86:89], v[230:233], v[146:149]
	v_mfma_f32_16x16x32_f16 v[120:123], v[86:89], v[234:237], v[120:123]
	v_mfma_f32_16x16x32_f16 v[124:127], v[90:93], v[222:225], v[124:127]
	v_mfma_f32_16x16x32_f16 v[146:149], v[90:93], v[226:229], v[150:153]
	v_mfma_f32_16x16x32_f16 v[134:137], v[90:93], v[234:237], v[134:137]
	v_mfma_f32_16x16x32_f16 v[150:153], v[90:93], v[230:233], v[154:157]
	s_setprio 0
	ds_read_b128 v[90:93], v251 offset:8192
	s_nop 0
	ds_read_b128 v[154:157], v251 offset:10240
	v_cvt_pk_f16_f32 v9, v56, v57
	v_cvt_pk_f16_f32 v8, v54, v55
	ds_write_b64 v100, v[8:9] offset:24576
	s_add_u32 s80, s22, 0xc0400
	s_addc_u32 s81, s90, 0
	global_load_dwordx4 v[86:89], v201, s[80:81] nt
	s_setprio 1
	s_waitcnt lgkmcnt(1)
	v_mfma_f32_16x16x32_f16 v[246:249], v[90:93], v[222:225], v[4:7]
	v_mfma_f32_16x16x32_f16 v[170:173], v[90:93], v[226:229], v[170:173]
	v_mfma_f32_16x16x32_f16 v[174:177], v[90:93], v[230:233], v[174:177]
	v_mfma_f32_16x16x32_f16 v[162:165], v[90:93], v[234:237], v[162:165]
	v_mfma_f32_16x16x32_f16 v[178:181], v[154:157], v[222:225], v[178:181]
	v_mfma_f32_16x16x32_f16 v[182:185], v[154:157], v[226:229], v[182:185]
	v_mfma_f32_16x16x32_f16 v[186:189], v[154:157], v[230:233], v[186:189]
	v_mfma_f32_16x16x32_f16 v[154:157], v[154:157], v[234:237], v[158:161]
	s_setprio 0
	ds_read_b128 v[4:7], v251 offset:12288
	ds_read_b128 v[54:57], v251 offset:14336
	v_cvt_pk_f16_f32 v9, v52, v53
	v_cvt_pk_f16_f32 v8, v50, v51
	ds_write_b64 v100, v[8:9] offset:28672
	s_add_u32 s80, s22, 0xe0400
	s_addc_u32 s81, s90, 0
	global_load_dwordx4 v[90:93], v201, s[80:81] nt
	s_setprio 1
	s_waitcnt lgkmcnt(1)
	v_mfma_f32_16x16x32_f16 v[66:69], v[4:7], v[222:225], v[66:69]
	v_mfma_f32_16x16x32_f16 v[158:161], v[4:7], v[226:229], v[210:213]
	v_mfma_f32_16x16x32_f16 v[210:213], v[4:7], v[230:233], v[214:217]
	v_mfma_f32_16x16x32_f16 v[166:169], v[4:7], v[234:237], v[166:169]
	v_mfma_f32_16x16x32_f16 v[190:193], v[54:57], v[222:225], v[190:193]
	v_mfma_f32_16x16x32_f16 v[202:205], v[54:57], v[226:229], v[202:205]
	v_mfma_f32_16x16x32_f16 v[206:209], v[54:57], v[230:233], v[206:209]
	v_mfma_f32_16x16x32_f16 v[214:217], v[54:57], v[234:237], v[218:221]
	s_setprio 0
	s_waitcnt vmcnt(4)
	s_waitcnt lgkmcnt(0)
	s_barrier
	s_nop 0
	ds_read_b128 v[218:221], v131
	ds_read_b128 v[222:225], v131 offset:2048
	ds_read_b128 v[226:229], v131 offset:4096
	ds_read_b128 v[230:233], v131 offset:6144
	ds_read_b128 v[50:53], v129
	ds_read_b128 v[54:57], v129 offset:2048
	s_add_u32 s80, s22, 0x500
	v_lshl_add_u64 v[8:9], s[30:31], 0, v[196:197]
	s_addc_u32 s81, s90, 0
	s_mov_b32 m0, s0
	v_cvt_pk_f16_f32 v5, v32, v33
	global_load_lds_dwordx4 v[8:9], off
	v_cvt_pk_f16_f32 v4, v30, v31
	ds_write_b64 v100, v[4:5] offset:32768
	global_load_dwordx4 v[4:7], v201, s[80:81] nt
	s_setprio 1
	s_waitcnt lgkmcnt(1)
	v_mfma_f32_16x16x32_f16 v[30:33], v[50:53], v[218:221], v[62:65]
	v_mfma_f32_16x16x32_f16 v[70:73], v[50:53], v[222:225], v[70:73]
	v_mfma_f32_16x16x32_f16 v[104:107], v[50:53], v[226:229], v[104:107]
	v_mfma_f32_16x16x32_f16 v[108:111], v[54:57], v[218:221], v[108:111]
	v_mfma_f32_16x16x32_f16 v[112:115], v[54:57], v[222:225], v[112:115]
	v_mfma_f32_16x16x32_f16 v[116:119], v[54:57], v[226:229], v[116:119]
	v_mfma_f32_16x16x32_f16 v[234:237], v[50:53], v[230:233], v[238:241]
	v_mfma_f32_16x16x32_f16 v[238:241], v[54:57], v[230:233], v[242:245]
	s_setprio 0
	ds_read_b128 v[54:57], v129 offset:4096
	ds_read_b128 v[62:65], v129 offset:6144
	s_mov_b32 m0, s1
	v_lshl_add_u64 v[50:51], v[8:9], 0, s[58:59]
	global_load_lds_dwordx4 v[50:51], off
	v_cvt_pk_f16_f32 v29, v28, v29
	v_cvt_pk_f16_f32 v28, v26, v27
	ds_write_b64 v100, v[28:29] offset:36864
	s_add_u32 s0, s22, 0x20500
	s_addc_u32 s1, s90, 0
	global_load_dwordx4 v[50:53], v201, s[0:1] nt
	s_setprio 1
	s_waitcnt lgkmcnt(1)
	v_mfma_f32_16x16x32_f16 v[26:29], v[54:57], v[218:221], v[58:61]
	v_mfma_f32_16x16x32_f16 v[120:123], v[54:57], v[230:233], v[120:123]
	v_mfma_f32_16x16x32_f16 v[124:127], v[62:65], v[218:221], v[124:127]
	v_mfma_f32_16x16x32_f16 v[146:149], v[62:65], v[222:225], v[146:149]
	v_mfma_f32_16x16x32_f16 v[134:137], v[62:65], v[230:233], v[134:137]
	v_mfma_f32_16x16x32_f16 v[138:141], v[54:57], v[222:225], v[138:141]
	v_mfma_f32_16x16x32_f16 v[142:145], v[54:57], v[226:229], v[142:145]
	v_mfma_f32_16x16x32_f16 v[150:153], v[62:65], v[226:229], v[150:153]
	s_setprio 0
	ds_read_b128 v[58:61], v129 offset:8192
	ds_read_b128 v[62:65], v129 offset:10240
	s_mov_b32 m0, s71
	v_lshl_add_u64 v[54:55], v[8:9], 0, s[60:61]
	global_load_lds_dwordx4 v[54:55], off
	v_cvt_pk_f16_f32 v25, v24, v25
	v_cvt_pk_f16_f32 v24, v22, v23
	ds_write_b64 v100, v[24:25] offset:40960
	s_add_u32 s0, s22, 0x40500
	s_addc_u32 s1, s90, 0
	global_load_dwordx4 v[54:57], v201, s[0:1] nt
	s_setprio 1
	s_waitcnt lgkmcnt(1)
	v_mfma_f32_16x16x32_f16 v[22:25], v[58:61], v[218:221], v[246:249]
	v_mfma_f32_16x16x32_f16 v[170:173], v[58:61], v[222:225], v[170:173]
	v_mfma_f32_16x16x32_f16 v[174:177], v[58:61], v[226:229], v[174:177]
	v_mfma_f32_16x16x32_f16 v[162:165], v[58:61], v[230:233], v[162:165]
	v_mfma_f32_16x16x32_f16 v[178:181], v[62:65], v[218:221], v[178:181]
	v_mfma_f32_16x16x32_f16 v[182:185], v[62:65], v[222:225], v[182:185]
	v_mfma_f32_16x16x32_f16 v[186:189], v[62:65], v[226:229], v[186:189]
	v_mfma_f32_16x16x32_f16 v[154:157], v[62:65], v[230:233], v[154:157]
	s_setprio 0
	ds_read_b128 v[62:65], v129 offset:12288
	ds_read_b128 v[242:245], v129 offset:14336
	s_mov_b32 m0, s72
	v_lshl_add_u64 v[8:9], v[8:9], 0, s[62:63]
	global_load_lds_dwordx4 v[8:9], off
	v_cvt_pk_f16_f32 v9, v20, v21
	v_cvt_pk_f16_f32 v8, v18, v19
	ds_write_b64 v100, v[8:9] offset:45056
	s_add_u32 s0, s22, 0x60500
	s_addc_u32 s1, s90, 0
	global_load_dwordx4 v[58:61], v201, s[0:1] nt
	s_setprio 1
	s_waitcnt lgkmcnt(1)
	v_mfma_f32_16x16x32_f16 v[18:21], v[62:65], v[218:221], v[66:69]
	v_mfma_f32_16x16x32_f16 v[158:161], v[62:65], v[222:225], v[158:161]
	v_mfma_f32_16x16x32_f16 v[210:213], v[62:65], v[226:229], v[210:213]
	v_mfma_f32_16x16x32_f16 v[166:169], v[62:65], v[230:233], v[166:169]
	v_mfma_f32_16x16x32_f16 v[190:193], v[242:245], v[218:221], v[190:193]
	v_mfma_f32_16x16x32_f16 v[202:205], v[242:245], v[222:225], v[202:205]
	v_mfma_f32_16x16x32_f16 v[206:209], v[242:245], v[226:229], v[206:209]
	v_mfma_f32_16x16x32_f16 v[214:217], v[242:245], v[230:233], v[214:217]
	s_setprio 0
	ds_read_b128 v[218:221], v128
	ds_read_b128 v[222:225], v128 offset:2048
	ds_read_b128 v[226:229], v128 offset:4096
	ds_read_b128 v[230:233], v128 offset:6144
	ds_read_b128 v[66:69], v130
	ds_read_b128 v[242:245], v130 offset:2048
	v_cvt_pk_f16_f32 v9, v16, v17
	v_cvt_pk_f16_f32 v8, v14, v15
	ds_write_b64 v100, v[8:9] offset:49152
	s_add_u32 s0, s22, 0x80500
	s_addc_u32 s1, s90, 0
	global_load_dwordx4 v[62:65], v201, s[0:1] nt
	s_setprio 1
	s_waitcnt lgkmcnt(1)
	v_mfma_f32_16x16x32_f16 v[14:17], v[66:69], v[218:221], v[30:33]
	v_mfma_f32_16x16x32_f16 v[30:33], v[66:69], v[222:225], v[70:73]
	v_mfma_f32_16x16x32_f16 v[104:107], v[66:69], v[226:229], v[104:107]
	v_mfma_f32_16x16x32_f16 v[108:111], v[242:245], v[218:221], v[108:111]
	v_mfma_f32_16x16x32_f16 v[112:115], v[242:245], v[222:225], v[112:115]
	v_mfma_f32_16x16x32_f16 v[116:119], v[242:245], v[226:229], v[116:119]
	v_mfma_f32_16x16x32_f16 v[234:237], v[66:69], v[230:233], v[234:237]
	v_mfma_f32_16x16x32_f16 v[238:241], v[242:245], v[230:233], v[238:241]
	s_setprio 0
	ds_read_b128 v[70:73], v130 offset:4096
	ds_read_b128 v[242:245], v130 offset:6144
	v_cvt_pk_f16_f32 v9, v12, v13
	v_cvt_pk_f16_f32 v8, v10, v11
	ds_write_b64 v100, v[8:9] offset:53248
	s_add_u32 s0, s22, 0xa0500
	s_addc_u32 s1, s90, 0
	global_load_dwordx4 v[66:69], v201, s[0:1] nt
	s_setprio 1
	s_waitcnt lgkmcnt(1)
	v_mfma_f32_16x16x32_f16 v[26:29], v[70:73], v[218:221], v[26:29]
	v_mfma_f32_16x16x32_f16 v[120:123], v[70:73], v[230:233], v[120:123]
	v_mfma_f32_16x16x32_f16 v[124:127], v[242:245], v[218:221], v[124:127]
	v_mfma_f32_16x16x32_f16 v[146:149], v[242:245], v[222:225], v[146:149]
	v_mfma_f32_16x16x32_f16 v[134:137], v[242:245], v[230:233], v[134:137]
	v_mfma_f32_16x16x32_f16 v[138:141], v[70:73], v[222:225], v[138:141]
	v_mfma_f32_16x16x32_f16 v[142:145], v[70:73], v[226:229], v[142:145]
	v_mfma_f32_16x16x32_f16 v[150:153], v[242:245], v[226:229], v[150:153]
	s_setprio 0
	ds_read_b128 v[8:11], v130 offset:8192
	ds_read_b128 v[242:245], v130 offset:10240
	v_cvt_pk_f16_f32 v13, v36, v37
	v_cvt_pk_f16_f32 v12, v34, v35
	ds_write_b64 v100, v[12:13] offset:57344
	s_add_u32 s0, s22, 0xc0500
	s_addc_u32 s1, s90, 0
	global_load_dwordx4 v[70:73], v201, s[0:1] nt
	s_setprio 1
	s_waitcnt lgkmcnt(1)
	v_mfma_f32_16x16x32_f16 v[22:25], v[8:11], v[218:221], v[22:25]
	v_mfma_f32_16x16x32_f16 v[170:173], v[8:11], v[222:225], v[170:173]
	v_mfma_f32_16x16x32_f16 v[174:177], v[8:11], v[226:229], v[174:177]
	v_mfma_f32_16x16x32_f16 v[162:165], v[8:11], v[230:233], v[162:165]
	v_mfma_f32_16x16x32_f16 v[178:181], v[242:245], v[218:221], v[178:181]
	v_mfma_f32_16x16x32_f16 v[182:185], v[242:245], v[222:225], v[182:185]
	v_mfma_f32_16x16x32_f16 v[186:189], v[242:245], v[226:229], v[186:189]
	v_mfma_f32_16x16x32_f16 v[154:157], v[242:245], v[230:233], v[154:157]
	s_setprio 0
	ds_read_b128 v[8:11], v130 offset:12288
	ds_read_b128 v[242:245], v130 offset:14336
	v_cvt_pk_f16_f32 v13, v40, v41
	v_cvt_pk_f16_f32 v12, v38, v39
	ds_write_b64 v100, v[12:13] offset:61440
	s_add_u32 s0, s22, 0xe0500
	s_addc_u32 s1, s90, 0
	global_load_dwordx4 v[36:39], v201, s[0:1] nt
	s_setprio 1
	s_waitcnt lgkmcnt(1)
	v_mfma_f32_16x16x32_f16 v[246:249], v[8:11], v[218:221], v[18:21]
	v_mfma_f32_16x16x32_f16 v[158:161], v[8:11], v[222:225], v[158:161]
	v_mfma_f32_16x16x32_f16 v[210:213], v[8:11], v[226:229], v[210:213]
	v_mfma_f32_16x16x32_f16 v[166:169], v[8:11], v[230:233], v[166:169]
	v_mfma_f32_16x16x32_f16 v[190:193], v[242:245], v[218:221], v[190:193]
	v_mfma_f32_16x16x32_f16 v[202:205], v[242:245], v[222:225], v[202:205]
	v_mfma_f32_16x16x32_f16 v[206:209], v[242:245], v[226:229], v[206:209]
	v_mfma_f32_16x16x32_f16 v[214:217], v[242:245], v[230:233], v[214:217]
	s_setprio 0
	s_waitcnt vmcnt(4)
	s_waitcnt lgkmcnt(0)
	s_barrier
	ds_read_b128 v[218:221], v131 offset:32768
	ds_read_b128 v[222:225], v131 offset:34816
	ds_read_b128 v[226:229], v131 offset:36864
	ds_read_b128 v[230:233], v131 offset:38912
	ds_read_b128 v[8:11], v129 offset:32768
	ds_read_b128 v[18:21], v129 offset:34816
	s_add_u32 s0, s22, 0x600
	s_addc_u32 s1, s90, 0
	v_lshl_add_u64 v[34:35], s[34:35], 0, v[196:197]
	s_mov_b32 m0, s70
	v_cvt_pk_f16_f32 v3, v2, v3
	global_load_lds_dwordx4 v[34:35], off
	v_cvt_pk_f16_f32 v2, v0, v1
	ds_write_b64 v100, v[2:3]
	global_load_dwordx4 v[0:3], v201, s[0:1] nt
	s_setprio 1
	s_waitcnt lgkmcnt(1)
	v_mfma_f32_16x16x32_f16 v[30:33], v[8:11], v[222:225], v[30:33]
	v_mfma_f32_16x16x32_f16 v[104:107], v[8:11], v[226:229], v[104:107]
	v_mfma_f32_16x16x32_f16 v[108:111], v[18:21], v[218:221], v[108:111]
	v_mfma_f32_16x16x32_f16 v[112:115], v[18:21], v[222:225], v[112:115]
	v_mfma_f32_16x16x32_f16 v[116:119], v[18:21], v[226:229], v[116:119]
	v_mfma_f32_16x16x32_f16 v[242:245], v[8:11], v[218:221], v[14:17]
	v_mfma_f32_16x16x32_f16 v[234:237], v[8:11], v[230:233], v[234:237]
	v_mfma_f32_16x16x32_f16 v[238:241], v[18:21], v[230:233], v[238:241]
	s_setprio 0
	ds_read_b128 v[12:15], v129 offset:36864
	ds_read_b128 v[16:19], v129 offset:38912
	s_mov_b32 m0, s73
	v_lshl_add_u64 v[8:9], v[34:35], 0, s[58:59]
	global_load_lds_dwordx4 v[8:9], off
	v_cvt_pk_f16_f32 v9, v44, v45
	v_cvt_pk_f16_f32 v8, v42, v43
	ds_write_b64 v100, v[8:9] offset:4096
	s_add_u32 s0, s22, 0x20600
	s_addc_u32 s1, s90, 0
	global_load_dwordx4 v[8:11], v201, s[0:1] nt
	s_setprio 1
	s_waitcnt lgkmcnt(1)
	v_mfma_f32_16x16x32_f16 v[40:43], v[12:15], v[218:221], v[26:29]
	v_mfma_f32_16x16x32_f16 v[120:123], v[12:15], v[230:233], v[120:123]
	v_mfma_f32_16x16x32_f16 v[124:127], v[16:19], v[218:221], v[124:127]
	v_mfma_f32_16x16x32_f16 v[146:149], v[16:19], v[222:225], v[146:149]
	v_mfma_f32_16x16x32_f16 v[134:137], v[16:19], v[230:233], v[134:137]
	v_mfma_f32_16x16x32_f16 v[138:141], v[12:15], v[222:225], v[138:141]
	v_mfma_f32_16x16x32_f16 v[142:145], v[12:15], v[226:229], v[142:145]
	v_mfma_f32_16x16x32_f16 v[150:153], v[16:19], v[226:229], v[150:153]
	s_setprio 0
	ds_read_b128 v[16:19], v129 offset:40960
	ds_read_b128 v[26:29], v129 offset:43008
	s_mov_b32 m0, s91
	v_lshl_add_u64 v[12:13], v[34:35], 0, s[60:61]
	global_load_lds_dwordx4 v[12:13], off
	v_cvt_pk_f16_f32 v13, v48, v49
	v_cvt_pk_f16_f32 v12, v46, v47
	ds_write_b64 v100, v[12:13] offset:8192
	s_add_u32 s0, s22, 0x40600
	s_addc_u32 s1, s90, 0
	global_load_dwordx4 v[12:15], v201, s[0:1] nt
	s_setprio 1
	s_waitcnt lgkmcnt(1)
	v_mfma_f32_16x16x32_f16 v[44:47], v[16:19], v[218:221], v[22:25]
	v_mfma_f32_16x16x32_f16 v[170:173], v[16:19], v[222:225], v[170:173]
	v_mfma_f32_16x16x32_f16 v[174:177], v[16:19], v[226:229], v[174:177]
	v_mfma_f32_16x16x32_f16 v[162:165], v[16:19], v[230:233], v[162:165]
	v_mfma_f32_16x16x32_f16 v[178:181], v[26:29], v[218:221], v[178:181]
	v_mfma_f32_16x16x32_f16 v[182:185], v[26:29], v[222:225], v[182:185]
	v_mfma_f32_16x16x32_f16 v[186:189], v[26:29], v[226:229], v[186:189]
	v_mfma_f32_16x16x32_f16 v[154:157], v[26:29], v[230:233], v[154:157]
	s_setprio 0
	ds_read_b128 v[20:23], v129 offset:45056
	ds_read_b128 v[24:27], v129 offset:47104
	s_mov_b32 m0, s92
	v_lshl_add_u64 v[16:17], v[34:35], 0, s[62:63]
	global_load_lds_dwordx4 v[16:17], off
	v_cvt_pk_f16_f32 v17, v76, v77
	v_cvt_pk_f16_f32 v16, v74, v75
	ds_write_b64 v100, v[16:17] offset:12288
	s_add_u32 s0, s22, 0x60600
	s_addc_u32 s1, s90, 0
	global_load_dwordx4 v[16:19], v201, s[0:1] nt
	s_setprio 1
	s_waitcnt lgkmcnt(1)
	v_mfma_f32_16x16x32_f16 v[74:77], v[20:23], v[218:221], v[246:249]
	v_mfma_f32_16x16x32_f16 v[158:161], v[20:23], v[222:225], v[158:161]
	v_mfma_f32_16x16x32_f16 v[210:213], v[20:23], v[226:229], v[210:213]
	v_mfma_f32_16x16x32_f16 v[166:169], v[20:23], v[230:233], v[166:169]
	v_mfma_f32_16x16x32_f16 v[190:193], v[24:27], v[218:221], v[190:193]
	v_mfma_f32_16x16x32_f16 v[202:205], v[24:27], v[222:225], v[202:205]
	v_mfma_f32_16x16x32_f16 v[206:209], v[24:27], v[226:229], v[206:209]
	v_mfma_f32_16x16x32_f16 v[214:217], v[24:27], v[230:233], v[214:217]
	s_setprio 0
	ds_read_b128 v[218:221], v128 offset:32768
	ds_read_b128 v[222:225], v128 offset:34816
	ds_read_b128 v[226:229], v128 offset:36864
	ds_read_b128 v[230:233], v128 offset:38912
	ds_read_b128 v[24:27], v130 offset:32768
	ds_read_b128 v[246:249], v130 offset:34816
	v_cvt_pk_f16_f32 v21, v80, v81
	v_cvt_pk_f16_f32 v20, v78, v79
	ds_write_b64 v100, v[20:21] offset:16384
	s_add_u32 s0, s22, 0x80600
	s_addc_u32 s1, s90, 0
	global_load_dwordx4 v[20:23], v201, s[0:1] nt
	s_setprio 1
	s_waitcnt lgkmcnt(1)
	v_mfma_f32_16x16x32_f16 v[78:81], v[24:27], v[218:221], v[242:245]
	v_mfma_f32_16x16x32_f16 v[104:107], v[24:27], v[226:229], v[104:107]
	v_mfma_f32_16x16x32_f16 v[108:111], v[246:249], v[218:221], v[108:111]
	v_mfma_f32_16x16x32_f16 v[112:115], v[246:249], v[222:225], v[112:115]
	v_mfma_f32_16x16x32_f16 v[116:119], v[246:249], v[226:229], v[116:119]
	v_mfma_f32_16x16x32_f16 v[242:245], v[24:27], v[222:225], v[30:33]
	v_mfma_f32_16x16x32_f16 v[234:237], v[24:27], v[230:233], v[234:237]
	v_mfma_f32_16x16x32_f16 v[238:241], v[246:249], v[230:233], v[238:241]
	s_setprio 0
	ds_read_b128 v[28:31], v130 offset:36864
	ds_read_b128 v[32:35], v130 offset:38912
	v_cvt_pk_f16_f32 v25, v84, v85
	v_cvt_pk_f16_f32 v24, v82, v83
	ds_write_b64 v100, v[24:25] offset:20480
	s_add_u32 s0, s22, 0xa0600
	s_addc_u32 s1, s90, 0
	global_load_dwordx4 v[24:27], v201, s[0:1] nt
	s_setprio 1
	s_waitcnt lgkmcnt(1)
	v_mfma_f32_16x16x32_f16 v[82:85], v[28:31], v[218:221], v[40:43]
	v_mfma_f32_16x16x32_f16 v[120:123], v[28:31], v[230:233], v[120:123]
	v_mfma_f32_16x16x32_f16 v[124:127], v[32:35], v[218:221], v[124:127]
	v_mfma_f32_16x16x32_f16 v[146:149], v[32:35], v[222:225], v[146:149]
	v_mfma_f32_16x16x32_f16 v[134:137], v[32:35], v[230:233], v[134:137]
	v_mfma_f32_16x16x32_f16 v[138:141], v[28:31], v[222:225], v[138:141]
	v_mfma_f32_16x16x32_f16 v[142:145], v[28:31], v[226:229], v[142:145]
	v_mfma_f32_16x16x32_f16 v[150:153], v[32:35], v[226:229], v[150:153]
	s_setprio 0
	ds_read_b128 v[32:35], v130 offset:40960
	ds_read_b128 v[40:43], v130 offset:43008
	v_cvt_pk_f16_f32 v29, v88, v89
	v_cvt_pk_f16_f32 v28, v86, v87
	ds_write_b64 v100, v[28:29] offset:24576
	s_add_u32 s0, s22, 0xc0600
	s_addc_u32 s1, s90, 0
	global_load_dwordx4 v[28:31], v201, s[0:1] nt
	s_setprio 1
	s_waitcnt lgkmcnt(1)
	v_mfma_f32_16x16x32_f16 v[86:89], v[32:35], v[218:221], v[44:47]
	v_mfma_f32_16x16x32_f16 v[170:173], v[32:35], v[222:225], v[170:173]
	v_mfma_f32_16x16x32_f16 v[174:177], v[32:35], v[226:229], v[174:177]
	v_mfma_f32_16x16x32_f16 v[162:165], v[32:35], v[230:233], v[162:165]
	v_mfma_f32_16x16x32_f16 v[178:181], v[40:43], v[218:221], v[178:181]
	v_mfma_f32_16x16x32_f16 v[182:185], v[40:43], v[222:225], v[182:185]
	v_mfma_f32_16x16x32_f16 v[186:189], v[40:43], v[226:229], v[186:189]
	v_mfma_f32_16x16x32_f16 v[154:157], v[40:43], v[230:233], v[154:157]
	s_setprio 0
	ds_read_b128 v[40:43], v130 offset:45056
	ds_read_b128 v[44:47], v130 offset:47104
	v_cvt_pk_f16_f32 v33, v92, v93
	v_cvt_pk_f16_f32 v32, v90, v91
	ds_write_b64 v100, v[32:33] offset:28672
	s_add_u32 s0, s22, 0xe0600
	s_addc_u32 s1, s90, 0
	global_load_dwordx4 v[32:35], v201, s[0:1] nt
	s_setprio 1
	s_waitcnt lgkmcnt(1)
	v_mfma_f32_16x16x32_f16 v[74:77], v[40:43], v[218:221], v[74:77]
	v_mfma_f32_16x16x32_f16 v[90:93], v[40:43], v[222:225], v[158:161]
	v_mfma_f32_16x16x32_f16 v[158:161], v[40:43], v[226:229], v[210:213]
	v_mfma_f32_16x16x32_f16 v[166:169], v[40:43], v[230:233], v[166:169]
	v_mfma_f32_16x16x32_f16 v[190:193], v[44:47], v[218:221], v[190:193]
	v_mfma_f32_16x16x32_f16 v[202:205], v[44:47], v[222:225], v[202:205]
	v_mfma_f32_16x16x32_f16 v[206:209], v[44:47], v[226:229], v[206:209]
	v_mfma_f32_16x16x32_f16 v[210:213], v[44:47], v[230:233], v[214:217]
	s_setprio 0
	s_waitcnt vmcnt(4)
	s_waitcnt lgkmcnt(0)
	s_barrier
	s_nop 0
	ds_read_b128 v[214:217], v131
	ds_read_b128 v[218:221], v131 offset:2048
	ds_read_b128 v[222:225], v131 offset:4096
	ds_read_b128 v[226:229], v131 offset:6144
	ds_read_b128 v[40:43], v129
	ds_read_b128 v[44:47], v129 offset:2048
	s_add_u32 s70, s22, 0x700
	s_addc_u32 s71, s90, 0
	v_lshl_add_u64 v[198:199], s[36:37], 0, v[196:197]
	v_readfirstlane_b32 s0, v95
	s_mov_b32 m0, s0
	v_cvt_pk_f16_f32 v7, v6, v7
	global_load_lds_dwordx4 v[198:199], off
	v_cvt_pk_f16_f32 v6, v4, v5
	ds_write_b64 v100, v[6:7] offset:32768
	global_load_dwordx4 v[4:7], v201, s[70:71] nt
	s_setprio 1
	s_waitcnt lgkmcnt(1)
	v_mfma_f32_16x16x32_f16 v[78:81], v[40:43], v[214:217], v[78:81]
	v_mfma_f32_16x16x32_f16 v[104:107], v[40:43], v[222:225], v[104:107]
	v_mfma_f32_16x16x32_f16 v[108:111], v[44:47], v[214:217], v[108:111]
	v_mfma_f32_16x16x32_f16 v[112:115], v[44:47], v[218:221], v[112:115]
	v_mfma_f32_16x16x32_f16 v[116:119], v[44:47], v[222:225], v[116:119]
	v_mfma_f32_16x16x32_f16 v[230:233], v[40:43], v[218:221], v[242:245]
	v_mfma_f32_16x16x32_f16 v[234:237], v[40:43], v[226:229], v[234:237]
	v_mfma_f32_16x16x32_f16 v[238:241], v[44:47], v[226:229], v[238:241]
	s_setprio 0
	ds_read_b128 v[44:47], v129 offset:4096
	ds_read_b128 v[242:245], v129 offset:6144
	v_readfirstlane_b32 s72, v96
	v_lshl_add_u64 v[40:41], v[198:199], 0, s[58:59]
	s_mov_b32 m0, s72
	s_nop 0
	global_load_lds_dwordx4 v[40:41], off
	v_cvt_pk_f16_f32 v41, v52, v53
	v_cvt_pk_f16_f32 v40, v50, v51
	ds_write_b64 v100, v[40:41] offset:36864
	s_add_u32 s70, s22, 0x20700
	s_addc_u32 s71, s90, 0
	global_load_dwordx4 v[40:43], v201, s[70:71] nt
	s_setprio 1
	s_waitcnt lgkmcnt(1)
	v_mfma_f32_16x16x32_f16 v[82:85], v[44:47], v[214:217], v[82:85]
	v_mfma_f32_16x16x32_f16 v[120:123], v[44:47], v[226:229], v[120:123]
	v_mfma_f32_16x16x32_f16 v[124:127], v[242:245], v[214:217], v[124:127]
	v_mfma_f32_16x16x32_f16 v[146:149], v[242:245], v[218:221], v[146:149]
	v_mfma_f32_16x16x32_f16 v[134:137], v[242:245], v[226:229], v[134:137]
	v_mfma_f32_16x16x32_f16 v[138:141], v[44:47], v[218:221], v[138:141]
	v_mfma_f32_16x16x32_f16 v[142:145], v[44:47], v[222:225], v[142:145]
	v_mfma_f32_16x16x32_f16 v[150:153], v[242:245], v[222:225], v[150:153]
	s_setprio 0
	ds_read_b128 v[48:51], v129 offset:8192
	ds_read_b128 v[242:245], v129 offset:10240
	v_readfirstlane_b32 s71, v97
	v_lshl_add_u64 v[44:45], v[198:199], 0, s[60:61]
	s_mov_b32 m0, s71
	s_nop 0
	global_load_lds_dwordx4 v[44:45], off
	v_cvt_pk_f16_f32 v45, v56, v57
	v_cvt_pk_f16_f32 v44, v54, v55
	ds_write_b64 v100, v[44:45] offset:40960
	s_add_u32 s80, s22, 0x40700
	s_addc_u32 s81, s90, 0
	global_load_dwordx4 v[44:47], v201, s[80:81] nt
	s_setprio 1
	s_waitcnt lgkmcnt(1)
	v_mfma_f32_16x16x32_f16 v[86:89], v[48:51], v[214:217], v[86:89]
	v_mfma_f32_16x16x32_f16 v[170:173], v[48:51], v[218:221], v[170:173]
	v_mfma_f32_16x16x32_f16 v[174:177], v[48:51], v[222:225], v[174:177]
	v_mfma_f32_16x16x32_f16 v[162:165], v[48:51], v[226:229], v[162:165]
	v_mfma_f32_16x16x32_f16 v[178:181], v[242:245], v[214:217], v[178:181]
	v_mfma_f32_16x16x32_f16 v[182:185], v[242:245], v[218:221], v[182:185]
	v_mfma_f32_16x16x32_f16 v[186:189], v[242:245], v[222:225], v[186:189]
	v_mfma_f32_16x16x32_f16 v[154:157], v[242:245], v[226:229], v[154:157]
	s_setprio 0
	ds_read_b128 v[52:55], v129 offset:12288
	ds_read_b128 v[242:245], v129 offset:14336
	v_readfirstlane_b32 s70, v98
	v_lshl_add_u64 v[48:49], v[198:199], 0, s[62:63]
	s_mov_b32 m0, s70
	s_nop 0
	global_load_lds_dwordx4 v[48:49], off
	v_cvt_pk_f16_f32 v49, v60, v61
	v_cvt_pk_f16_f32 v48, v58, v59
	ds_write_b64 v100, v[48:49] offset:45056
	s_add_u32 s80, s22, 0x60700
	s_addc_u32 s81, s90, 0
	global_load_dwordx4 v[48:51], v201, s[80:81] nt
	s_setprio 1
	s_waitcnt lgkmcnt(1)
	v_mfma_f32_16x16x32_f16 v[74:77], v[52:55], v[214:217], v[74:77]
	v_mfma_f32_16x16x32_f16 v[90:93], v[52:55], v[218:221], v[90:93]
	v_mfma_f32_16x16x32_f16 v[158:161], v[52:55], v[222:225], v[158:161]
	v_mfma_f32_16x16x32_f16 v[166:169], v[52:55], v[226:229], v[166:169]
	v_mfma_f32_16x16x32_f16 v[190:193], v[242:245], v[214:217], v[190:193]
	v_mfma_f32_16x16x32_f16 v[202:205], v[242:245], v[218:221], v[202:205]
	v_mfma_f32_16x16x32_f16 v[206:209], v[242:245], v[222:225], v[206:209]
	v_mfma_f32_16x16x32_f16 v[210:213], v[242:245], v[226:229], v[210:213]
	s_setprio 0
	ds_read_b128 v[214:217], v128
	ds_read_b128 v[218:221], v128 offset:2048
	ds_read_b128 v[222:225], v128 offset:4096
	ds_read_b128 v[226:229], v128 offset:6144
	ds_read_b128 v[56:59], v130
	ds_read_b128 v[242:245], v130 offset:2048
	v_cvt_pk_f16_f32 v53, v64, v65
	v_cvt_pk_f16_f32 v52, v62, v63
	ds_write_b64 v100, v[52:53] offset:49152
	s_add_u32 s80, s22, 0x80700
	s_addc_u32 s81, s90, 0
	global_load_dwordx4 v[52:55], v201, s[80:81] nt
	s_setprio 1
	s_waitcnt lgkmcnt(1)
	v_mfma_f32_16x16x32_f16 v[78:81], v[56:59], v[214:217], v[78:81]
	v_mfma_f32_16x16x32_f16 v[104:107], v[56:59], v[222:225], v[104:107]
	v_mfma_f32_16x16x32_f16 v[108:111], v[242:245], v[214:217], v[108:111]
	v_mfma_f32_16x16x32_f16 v[112:115], v[242:245], v[218:221], v[112:115]
	v_mfma_f32_16x16x32_f16 v[116:119], v[242:245], v[222:225], v[116:119]
	v_mfma_f32_16x16x32_f16 v[230:233], v[56:59], v[218:221], v[230:233]
	v_mfma_f32_16x16x32_f16 v[234:237], v[56:59], v[226:229], v[234:237]
	v_mfma_f32_16x16x32_f16 v[238:241], v[242:245], v[226:229], v[238:241]
	s_setprio 0
	ds_read_b128 v[60:63], v130 offset:4096
	ds_read_b128 v[242:245], v130 offset:6144
	v_cvt_pk_f16_f32 v57, v68, v69
	v_cvt_pk_f16_f32 v56, v66, v67
	ds_write_b64 v100, v[56:57] offset:53248
	s_add_u32 s80, s22, 0xa0700
	s_addc_u32 s81, s90, 0
	global_load_dwordx4 v[56:59], v201, s[80:81] nt
	s_setprio 1
	s_waitcnt lgkmcnt(1)
	v_mfma_f32_16x16x32_f16 v[82:85], v[60:63], v[214:217], v[82:85]
	v_mfma_f32_16x16x32_f16 v[120:123], v[60:63], v[226:229], v[120:123]
	v_mfma_f32_16x16x32_f16 v[124:127], v[242:245], v[214:217], v[124:127]
	v_mfma_f32_16x16x32_f16 v[146:149], v[242:245], v[218:221], v[146:149]
	v_mfma_f32_16x16x32_f16 v[134:137], v[242:245], v[226:229], v[134:137]
	v_mfma_f32_16x16x32_f16 v[138:141], v[60:63], v[218:221], v[138:141]
	v_mfma_f32_16x16x32_f16 v[142:145], v[60:63], v[222:225], v[142:145]
	v_mfma_f32_16x16x32_f16 v[150:153], v[242:245], v[222:225], v[150:153]
	s_setprio 0
	ds_read_b128 v[64:67], v130 offset:8192
	ds_read_b128 v[242:245], v130 offset:10240
	v_cvt_pk_f16_f32 v61, v72, v73
	v_cvt_pk_f16_f32 v60, v70, v71
	ds_write_b64 v100, v[60:61] offset:57344
	s_add_u32 s80, s22, 0xc0700
	s_addc_u32 s81, s90, 0
	global_load_dwordx4 v[60:63], v201, s[80:81] nt
	s_setprio 1
	s_waitcnt lgkmcnt(1)
	v_mfma_f32_16x16x32_f16 v[86:89], v[64:67], v[214:217], v[86:89]
	v_mfma_f32_16x16x32_f16 v[170:173], v[64:67], v[218:221], v[170:173]
	v_mfma_f32_16x16x32_f16 v[174:177], v[64:67], v[222:225], v[174:177]
	v_mfma_f32_16x16x32_f16 v[162:165], v[64:67], v[226:229], v[162:165]
	v_mfma_f32_16x16x32_f16 v[178:181], v[242:245], v[214:217], v[178:181]
	v_mfma_f32_16x16x32_f16 v[182:185], v[242:245], v[218:221], v[182:185]
	v_mfma_f32_16x16x32_f16 v[186:189], v[242:245], v[222:225], v[186:189]
	v_mfma_f32_16x16x32_f16 v[154:157], v[242:245], v[226:229], v[154:157]
	s_setprio 0
	ds_read_b128 v[64:67], v130 offset:12288
	ds_read_b128 v[68:71], v130 offset:14336
	v_cvt_pk_f16_f32 v39, v38, v39
	v_cvt_pk_f16_f32 v38, v36, v37
	ds_write_b64 v100, v[38:39] offset:61440
	s_add_u32 s80, s22, 0xe0700
	s_addc_u32 s81, s90, 0
	global_load_dwordx4 v[36:39], v201, s[80:81] nt
	s_setprio 1
	s_waitcnt lgkmcnt(1)
	v_mfma_f32_16x16x32_f16 v[90:93], v[64:67], v[218:221], v[90:93]
	v_mfma_f32_16x16x32_f16 v[242:245], v[64:67], v[214:217], v[74:77]
	v_mfma_f32_16x16x32_f16 v[158:161], v[64:67], v[222:225], v[158:161]
	v_mfma_f32_16x16x32_f16 v[166:169], v[64:67], v[226:229], v[166:169]
	v_mfma_f32_16x16x32_f16 v[190:193], v[68:71], v[214:217], v[190:193]
	v_mfma_f32_16x16x32_f16 v[202:205], v[68:71], v[218:221], v[202:205]
	v_mfma_f32_16x16x32_f16 v[206:209], v[68:71], v[222:225], v[206:209]
	v_mfma_f32_16x16x32_f16 v[210:213], v[68:71], v[226:229], v[210:213]
	s_setprio 0
	s_waitcnt vmcnt(4)
	s_waitcnt lgkmcnt(0)
	s_barrier
	ds_read_b128 v[214:217], v131 offset:32768
	ds_read_b128 v[218:221], v131 offset:34816
	ds_read_b128 v[222:225], v131 offset:36864
	ds_read_b128 v[226:229], v131 offset:38912
	ds_read_b128 v[64:67], v129 offset:32768
	ds_read_b128 v[68:71], v129 offset:34816
	s_add_u32 s80, s22, 0x800
	s_addc_u32 s81, s90, 0
	v_lshl_add_u64 v[198:199], s[38:39], 0, v[196:197]
	v_readfirstlane_b32 s1, v94
	s_mov_b32 m0, s1
	v_cvt_pk_f16_f32 v3, v2, v3
	global_load_lds_dwordx4 v[198:199], off
	v_cvt_pk_f16_f32 v2, v0, v1
	ds_write_b64 v100, v[2:3]
	global_load_dwordx4 v[0:3], v201, s[80:81] nt
	s_setprio 1
	s_waitcnt lgkmcnt(1)
	v_mfma_f32_16x16x32_f16 v[104:107], v[64:67], v[222:225], v[104:107]
	v_mfma_f32_16x16x32_f16 v[108:111], v[68:71], v[214:217], v[108:111]
	v_mfma_f32_16x16x32_f16 v[112:115], v[68:71], v[218:221], v[112:115]
	v_mfma_f32_16x16x32_f16 v[116:119], v[68:71], v[222:225], v[116:119]
	v_mfma_f32_16x16x32_f16 v[246:249], v[64:67], v[214:217], v[78:81]
	v_mfma_f32_16x16x32_f16 v[230:233], v[64:67], v[218:221], v[230:233]
	v_mfma_f32_16x16x32_f16 v[234:237], v[64:67], v[226:229], v[234:237]
	v_mfma_f32_16x16x32_f16 v[238:241], v[68:71], v[226:229], v[238:241]
	s_setprio 0
	ds_read_b128 v[68:71], v129 offset:36864
	ds_read_b128 v[72:75], v129 offset:38912
	v_readfirstlane_b32 s92, v99
	v_lshl_add_u64 v[64:65], v[198:199], 0, s[58:59]
	s_mov_b32 m0, s92
	v_cvt_pk_f16_f32 v11, v10, v11
	global_load_lds_dwordx4 v[64:65], off
	v_cvt_pk_f16_f32 v10, v8, v9
	ds_write_b64 v100, v[10:11] offset:4096
	s_add_u32 s80, s22, 0x20800
	s_addc_u32 s81, s90, 0
	global_load_dwordx4 v[64:67], v201, s[80:81] nt
	s_setprio 1
	s_waitcnt lgkmcnt(1)
	v_mfma_f32_16x16x32_f16 v[8:11], v[68:71], v[214:217], v[82:85]
	v_mfma_f32_16x16x32_f16 v[120:123], v[68:71], v[226:229], v[120:123]
	v_mfma_f32_16x16x32_f16 v[124:127], v[72:75], v[214:217], v[124:127]
	v_mfma_f32_16x16x32_f16 v[146:149], v[72:75], v[218:221], v[146:149]
	v_mfma_f32_16x16x32_f16 v[134:137], v[72:75], v[226:229], v[134:137]
	v_mfma_f32_16x16x32_f16 v[138:141], v[68:71], v[218:221], v[138:141]
	v_mfma_f32_16x16x32_f16 v[142:145], v[68:71], v[222:225], v[142:145]
	v_mfma_f32_16x16x32_f16 v[150:153], v[72:75], v[222:225], v[150:153]
	s_setprio 0
	ds_read_b128 v[72:75], v129 offset:40960
	ds_read_b128 v[76:79], v129 offset:43008
	v_readfirstlane_b32 s91, v101
	v_lshl_add_u64 v[68:69], v[198:199], 0, s[60:61]
	s_mov_b32 m0, s91
	v_cvt_pk_f16_f32 v15, v14, v15
	global_load_lds_dwordx4 v[68:69], off
	v_cvt_pk_f16_f32 v14, v12, v13
	ds_write_b64 v100, v[14:15] offset:8192
	s_add_u32 s80, s22, 0x40800
	s_addc_u32 s81, s90, 0
	global_load_dwordx4 v[68:71], v201, s[80:81] nt
	s_setprio 1
	s_waitcnt lgkmcnt(1)
	v_mfma_f32_16x16x32_f16 v[12:15], v[72:75], v[214:217], v[86:89]
	v_mfma_f32_16x16x32_f16 v[170:173], v[72:75], v[218:221], v[170:173]
	v_mfma_f32_16x16x32_f16 v[174:177], v[72:75], v[222:225], v[174:177]
	v_mfma_f32_16x16x32_f16 v[162:165], v[72:75], v[226:229], v[162:165]
	v_mfma_f32_16x16x32_f16 v[178:181], v[76:79], v[214:217], v[178:181]
	v_mfma_f32_16x16x32_f16 v[182:185], v[76:79], v[218:221], v[182:185]
	v_mfma_f32_16x16x32_f16 v[186:189], v[76:79], v[222:225], v[186:189]
	v_mfma_f32_16x16x32_f16 v[154:157], v[76:79], v[226:229], v[154:157]
	s_setprio 0
	ds_read_b128 v[76:79], v129 offset:45056
	ds_read_b128 v[80:83], v129 offset:47104
	v_readfirstlane_b32 s73, v102
	v_lshl_add_u64 v[72:73], v[198:199], 0, s[62:63]
	s_mov_b32 m0, s73
	v_cvt_pk_f16_f32 v19, v18, v19
	global_load_lds_dwordx4 v[72:73], off
	v_cvt_pk_f16_f32 v18, v16, v17
	ds_write_b64 v100, v[18:19] offset:12288
	s_add_u32 s80, s22, 0x60800
	s_addc_u32 s81, s90, 0
	global_load_dwordx4 v[72:75], v201, s[80:81] nt
	s_setprio 1
	s_waitcnt lgkmcnt(1)
	v_mfma_f32_16x16x32_f16 v[16:19], v[76:79], v[214:217], v[242:245]
	v_mfma_f32_16x16x32_f16 v[242:245], v[76:79], v[218:221], v[90:93]
	v_mfma_f32_16x16x32_f16 v[158:161], v[76:79], v[222:225], v[158:161]
	v_mfma_f32_16x16x32_f16 v[166:169], v[76:79], v[226:229], v[166:169]
	v_mfma_f32_16x16x32_f16 v[190:193], v[80:83], v[214:217], v[190:193]
	v_mfma_f32_16x16x32_f16 v[202:205], v[80:83], v[218:221], v[202:205]
	v_mfma_f32_16x16x32_f16 v[206:209], v[80:83], v[222:225], v[206:209]
	v_mfma_f32_16x16x32_f16 v[210:213], v[80:83], v[226:229], v[210:213]
	s_setprio 0
	ds_read_b128 v[214:217], v128 offset:32768
	ds_read_b128 v[218:221], v128 offset:34816
	ds_read_b128 v[222:225], v128 offset:36864
	ds_read_b128 v[226:229], v128 offset:38912
	ds_read_b128 v[80:83], v130 offset:32768
	ds_read_b128 v[84:87], v130 offset:34816
	v_cvt_pk_f16_f32 v23, v22, v23
	v_cvt_pk_f16_f32 v22, v20, v21
	ds_write_b64 v100, v[22:23] offset:16384
	s_add_u32 s80, s22, 0x80800
	s_addc_u32 s81, s90, 0
	global_load_dwordx4 v[76:79], v201, s[80:81] nt
	s_setprio 1
	s_waitcnt lgkmcnt(1)
	v_mfma_f32_16x16x32_f16 v[20:23], v[80:83], v[214:217], v[246:249]
	v_mfma_f32_16x16x32_f16 v[104:107], v[80:83], v[222:225], v[104:107]
	v_mfma_f32_16x16x32_f16 v[108:111], v[84:87], v[214:217], v[108:111]
	v_mfma_f32_16x16x32_f16 v[112:115], v[84:87], v[218:221], v[112:115]
	v_mfma_f32_16x16x32_f16 v[116:119], v[84:87], v[222:225], v[116:119]
	v_mfma_f32_16x16x32_f16 v[230:233], v[80:83], v[218:221], v[230:233]
	v_mfma_f32_16x16x32_f16 v[234:237], v[80:83], v[226:229], v[234:237]
	v_mfma_f32_16x16x32_f16 v[238:241], v[84:87], v[226:229], v[238:241]
	s_setprio 0
	ds_read_b128 v[84:87], v130 offset:36864
	ds_read_b128 v[88:91], v130 offset:38912
	v_cvt_pk_f16_f32 v27, v26, v27
	v_cvt_pk_f16_f32 v26, v24, v25
	ds_write_b64 v100, v[26:27] offset:20480
	s_add_u32 s80, s22, 0xa0800
	s_addc_u32 s81, s90, 0
	global_load_dwordx4 v[80:83], v201, s[80:81] nt
	s_setprio 1
	s_waitcnt lgkmcnt(1)
	v_mfma_f32_16x16x32_f16 v[24:27], v[84:87], v[214:217], v[8:11]
	v_mfma_f32_16x16x32_f16 v[120:123], v[84:87], v[226:229], v[120:123]
	v_mfma_f32_16x16x32_f16 v[124:127], v[88:91], v[214:217], v[124:127]
	v_mfma_f32_16x16x32_f16 v[146:149], v[88:91], v[218:221], v[146:149]
	v_mfma_f32_16x16x32_f16 v[134:137], v[88:91], v[226:229], v[134:137]
	v_mfma_f32_16x16x32_f16 v[138:141], v[84:87], v[218:221], v[138:141]
	v_mfma_f32_16x16x32_f16 v[142:145], v[84:87], v[222:225], v[142:145]
	v_mfma_f32_16x16x32_f16 v[150:153], v[88:91], v[222:225], v[150:153]
	s_setprio 0
	ds_read_b128 v[8:11], v130 offset:40960
	ds_read_b128 v[88:91], v130 offset:43008
	v_cvt_pk_f16_f32 v31, v30, v31
	v_cvt_pk_f16_f32 v30, v28, v29
	ds_write_b64 v100, v[30:31] offset:24576
	s_add_u32 s80, s22, 0xc0800
	s_addc_u32 s81, s90, 0
	global_load_dwordx4 v[84:87], v201, s[80:81] nt
	s_setprio 1
	s_waitcnt lgkmcnt(1)
	v_mfma_f32_16x16x32_f16 v[12:15], v[8:11], v[214:217], v[12:15]
	v_mfma_f32_16x16x32_f16 v[28:31], v[8:11], v[218:221], v[170:173]
	v_mfma_f32_16x16x32_f16 v[170:173], v[8:11], v[222:225], v[174:177]
	v_mfma_f32_16x16x32_f16 v[162:165], v[8:11], v[226:229], v[162:165]
	v_mfma_f32_16x16x32_f16 v[174:177], v[88:91], v[214:217], v[178:181]
	v_mfma_f32_16x16x32_f16 v[178:181], v[88:91], v[218:221], v[182:185]
	v_mfma_f32_16x16x32_f16 v[182:185], v[88:91], v[222:225], v[186:189]
	v_mfma_f32_16x16x32_f16 v[154:157], v[88:91], v[226:229], v[154:157]
	s_setprio 0
	ds_read_b128 v[8:11], v130 offset:45056
	ds_read_b128 v[186:189], v130 offset:47104
	v_cvt_pk_f16_f32 v35, v34, v35
	v_cvt_pk_f16_f32 v34, v32, v33
	ds_write_b64 v100, v[34:35] offset:28672
	s_add_u32 s80, s22, 0xe0800
	s_addc_u32 s81, s90, 0
	global_load_dwordx4 v[88:91], v201, s[80:81] nt
	s_setprio 1
	s_waitcnt lgkmcnt(1)
	v_mfma_f32_16x16x32_f16 v[16:19], v[8:11], v[214:217], v[16:19]
	v_mfma_f32_16x16x32_f16 v[32:35], v[8:11], v[218:221], v[242:245]
	v_mfma_f32_16x16x32_f16 v[158:161], v[8:11], v[222:225], v[158:161]
	v_mfma_f32_16x16x32_f16 v[166:169], v[8:11], v[226:229], v[166:169]
	v_mfma_f32_16x16x32_f16 v[190:193], v[186:189], v[214:217], v[190:193]
	v_mfma_f32_16x16x32_f16 v[202:205], v[186:189], v[218:221], v[202:205]
	v_mfma_f32_16x16x32_f16 v[206:209], v[186:189], v[222:225], v[206:209]
	v_mfma_f32_16x16x32_f16 v[186:189], v[186:189], v[226:229], v[210:213]
	s_setprio 0
	s_waitcnt vmcnt(4)
	s_waitcnt lgkmcnt(0)
	s_barrier
	s_nop 0
	ds_read_b128 v[210:213], v131
	ds_read_b128 v[214:217], v131 offset:2048
	ds_read_b128 v[218:221], v131 offset:4096
	ds_read_b128 v[222:225], v131 offset:6144
	ds_read_b128 v[8:11], v129
	ds_read_b128 v[226:229], v129 offset:2048
	s_add_u32 s80, s22, 0x900
	v_lshl_add_u64 v[92:93], s[40:41], 0, v[196:197]
	s_addc_u32 s81, s90, 0
	s_mov_b32 m0, s0
	v_cvt_pk_f16_f32 v7, v6, v7
	global_load_lds_dwordx4 v[92:93], off
	v_cvt_pk_f16_f32 v6, v4, v5
	ds_write_b64 v100, v[6:7] offset:32768
	global_load_dwordx4 v[4:7], v201, s[80:81] nt
	s_setprio 1
	s_waitcnt lgkmcnt(1)
	v_mfma_f32_16x16x32_f16 v[20:23], v[8:11], v[210:213], v[20:23]
	v_mfma_f32_16x16x32_f16 v[104:107], v[8:11], v[218:221], v[104:107]
	v_mfma_f32_16x16x32_f16 v[108:111], v[226:229], v[210:213], v[108:111]
	v_mfma_f32_16x16x32_f16 v[112:115], v[226:229], v[214:217], v[112:115]
	v_mfma_f32_16x16x32_f16 v[116:119], v[226:229], v[218:221], v[116:119]
	v_mfma_f32_16x16x32_f16 v[230:233], v[8:11], v[214:217], v[230:233]
	v_mfma_f32_16x16x32_f16 v[234:237], v[8:11], v[222:225], v[234:237]
	v_mfma_f32_16x16x32_f16 v[226:229], v[226:229], v[222:225], v[238:241]
	s_setprio 0
	s_nop 1
	ds_read_b128 v[238:241], v129 offset:4096
	ds_read_b128 v[242:245], v129 offset:6144
	s_mov_b32 m0, s72
	v_lshl_add_u64 v[8:9], v[92:93], 0, s[58:59]
	global_load_lds_dwordx4 v[8:9], off
	v_cvt_pk_f16_f32 v9, v42, v43
	v_cvt_pk_f16_f32 v8, v40, v41
	ds_write_b64 v100, v[8:9] offset:36864
	s_add_u32 s80, s22, 0x20900
	s_addc_u32 s81, s90, 0
	global_load_dwordx4 v[8:11], v201, s[80:81] nt
	s_setprio 1
	s_waitcnt lgkmcnt(1)
	v_mfma_f32_16x16x32_f16 v[24:27], v[238:241], v[210:213], v[24:27]
	v_mfma_f32_16x16x32_f16 v[120:123], v[238:241], v[222:225], v[120:123]
	v_mfma_f32_16x16x32_f16 v[124:127], v[242:245], v[210:213], v[124:127]
	v_mfma_f32_16x16x32_f16 v[146:149], v[242:245], v[214:217], v[146:149]
	v_mfma_f32_16x16x32_f16 v[134:137], v[242:245], v[222:225], v[134:137]
	v_mfma_f32_16x16x32_f16 v[138:141], v[238:241], v[214:217], v[138:141]
	v_mfma_f32_16x16x32_f16 v[142:145], v[238:241], v[218:221], v[142:145]
	v_mfma_f32_16x16x32_f16 v[150:153], v[242:245], v[218:221], v[150:153]
	s_setprio 0
	ds_read_b128 v[238:241], v129 offset:8192
	ds_read_b128 v[242:245], v129 offset:10240
	s_mov_b32 m0, s71
	v_lshl_add_u64 v[40:41], v[92:93], 0, s[60:61]
	global_load_lds_dwordx4 v[40:41], off
	v_cvt_pk_f16_f32 v41, v46, v47
	v_cvt_pk_f16_f32 v40, v44, v45
	ds_write_b64 v100, v[40:41] offset:40960
	s_add_u32 s80, s22, 0x40900
	s_addc_u32 s81, s90, 0
	global_load_dwordx4 v[40:43], v201, s[80:81] nt
	s_setprio 1
	s_waitcnt lgkmcnt(1)
	v_mfma_f32_16x16x32_f16 v[12:15], v[238:241], v[210:213], v[12:15]
	v_mfma_f32_16x16x32_f16 v[28:31], v[238:241], v[214:217], v[28:31]
	v_mfma_f32_16x16x32_f16 v[170:173], v[238:241], v[218:221], v[170:173]
	v_mfma_f32_16x16x32_f16 v[162:165], v[238:241], v[222:225], v[162:165]
	v_mfma_f32_16x16x32_f16 v[174:177], v[242:245], v[210:213], v[174:177]
	v_mfma_f32_16x16x32_f16 v[178:181], v[242:245], v[214:217], v[178:181]
	v_mfma_f32_16x16x32_f16 v[182:185], v[242:245], v[218:221], v[182:185]
	v_mfma_f32_16x16x32_f16 v[154:157], v[242:245], v[222:225], v[154:157]
	s_setprio 0
	ds_read_b128 v[238:241], v129 offset:12288
	ds_read_b128 v[242:245], v129 offset:14336
	s_mov_b32 m0, s70
	v_lshl_add_u64 v[44:45], v[92:93], 0, s[62:63]
	global_load_lds_dwordx4 v[44:45], off
	v_cvt_pk_f16_f32 v45, v50, v51
	v_cvt_pk_f16_f32 v44, v48, v49
	ds_write_b64 v100, v[44:45] offset:45056
	s_add_u32 s70, s22, 0x60900
	s_addc_u32 s71, s90, 0
	global_load_dwordx4 v[44:47], v201, s[70:71] nt
	s_setprio 1
	s_waitcnt lgkmcnt(1)
	v_mfma_f32_16x16x32_f16 v[16:19], v[238:241], v[210:213], v[16:19]
	v_mfma_f32_16x16x32_f16 v[32:35], v[238:241], v[214:217], v[32:35]
	v_mfma_f32_16x16x32_f16 v[158:161], v[238:241], v[218:221], v[158:161]
	v_mfma_f32_16x16x32_f16 v[166:169], v[238:241], v[222:225], v[166:169]
	v_mfma_f32_16x16x32_f16 v[190:193], v[242:245], v[210:213], v[190:193]
	v_mfma_f32_16x16x32_f16 v[202:205], v[242:245], v[214:217], v[202:205]
	v_mfma_f32_16x16x32_f16 v[206:209], v[242:245], v[218:221], v[206:209]
	v_mfma_f32_16x16x32_f16 v[186:189], v[242:245], v[222:225], v[186:189]
	s_setprio 0
	ds_read_b128 v[210:213], v128
	ds_read_b128 v[214:217], v128 offset:2048
	ds_read_b128 v[218:221], v128 offset:4096
	ds_read_b128 v[222:225], v128 offset:6144
	ds_read_b128 v[238:241], v130
	ds_read_b128 v[242:245], v130 offset:2048
	v_cvt_pk_f16_f32 v49, v54, v55
	v_cvt_pk_f16_f32 v48, v52, v53
	ds_write_b64 v100, v[48:49] offset:49152
	s_add_u32 s70, s22, 0x80900
	s_addc_u32 s71, s90, 0
	global_load_dwordx4 v[48:51], v201, s[70:71] nt
	s_setprio 1
	s_waitcnt lgkmcnt(1)
	v_mfma_f32_16x16x32_f16 v[20:23], v[238:241], v[210:213], v[20:23]
	v_mfma_f32_16x16x32_f16 v[104:107], v[238:241], v[218:221], v[104:107]
	v_mfma_f32_16x16x32_f16 v[108:111], v[242:245], v[210:213], v[108:111]
	v_mfma_f32_16x16x32_f16 v[112:115], v[242:245], v[214:217], v[112:115]
	v_mfma_f32_16x16x32_f16 v[116:119], v[242:245], v[218:221], v[116:119]
	v_mfma_f32_16x16x32_f16 v[230:233], v[238:241], v[214:217], v[230:233]
	v_mfma_f32_16x16x32_f16 v[234:237], v[238:241], v[222:225], v[234:237]
	v_mfma_f32_16x16x32_f16 v[226:229], v[242:245], v[222:225], v[226:229]
	s_setprio 0
	ds_read_b128 v[238:241], v130 offset:4096
	ds_read_b128 v[242:245], v130 offset:6144
	v_cvt_pk_f16_f32 v53, v58, v59
	v_cvt_pk_f16_f32 v52, v56, v57
	ds_write_b64 v100, v[52:53] offset:53248
	s_add_u32 s70, s22, 0xa0900
	s_addc_u32 s71, s90, 0
	global_load_dwordx4 v[52:55], v201, s[70:71] nt
	s_setprio 1
	s_waitcnt lgkmcnt(1)
	v_mfma_f32_16x16x32_f16 v[24:27], v[238:241], v[210:213], v[24:27]
	v_mfma_f32_16x16x32_f16 v[120:123], v[238:241], v[222:225], v[120:123]
	v_mfma_f32_16x16x32_f16 v[124:127], v[242:245], v[210:213], v[124:127]
	v_mfma_f32_16x16x32_f16 v[146:149], v[242:245], v[214:217], v[146:149]
	v_mfma_f32_16x16x32_f16 v[134:137], v[242:245], v[222:225], v[134:137]
	v_mfma_f32_16x16x32_f16 v[138:141], v[238:241], v[214:217], v[138:141]
	v_mfma_f32_16x16x32_f16 v[142:145], v[238:241], v[218:221], v[142:145]
	v_mfma_f32_16x16x32_f16 v[150:153], v[242:245], v[218:221], v[150:153]
	s_setprio 0
	ds_read_b128 v[238:241], v130 offset:8192
	ds_read_b128 v[242:245], v130 offset:10240
	v_cvt_pk_f16_f32 v57, v62, v63
	v_cvt_pk_f16_f32 v56, v60, v61
	ds_write_b64 v100, v[56:57] offset:57344
	s_add_u32 s70, s22, 0xc0900
	s_addc_u32 s71, s90, 0
	global_load_dwordx4 v[56:59], v201, s[70:71] nt
	s_setprio 1
	s_waitcnt lgkmcnt(1)
	v_mfma_f32_16x16x32_f16 v[28:31], v[238:241], v[214:217], v[28:31]
	v_mfma_f32_16x16x32_f16 v[246:249], v[238:241], v[210:213], v[12:15]
	v_mfma_f32_16x16x32_f16 v[170:173], v[238:241], v[218:221], v[170:173]
	v_mfma_f32_16x16x32_f16 v[162:165], v[238:241], v[222:225], v[162:165]
	v_mfma_f32_16x16x32_f16 v[174:177], v[242:245], v[210:213], v[174:177]
	v_mfma_f32_16x16x32_f16 v[178:181], v[242:245], v[214:217], v[178:181]
	v_mfma_f32_16x16x32_f16 v[182:185], v[242:245], v[218:221], v[182:185]
	v_mfma_f32_16x16x32_f16 v[154:157], v[242:245], v[222:225], v[154:157]
	s_setprio 0
	ds_read_b128 v[12:15], v130 offset:12288
	ds_read_b128 v[238:241], v130 offset:14336
	v_cvt_pk_f16_f32 v39, v38, v39
	v_cvt_pk_f16_f32 v38, v36, v37
	ds_write_b64 v100, v[38:39] offset:61440
	s_add_u32 s70, s22, 0xe0900
	s_addc_u32 s71, s90, 0
	global_load_dwordx4 v[60:63], v201, s[70:71] nt
	s_setprio 1
	s_waitcnt lgkmcnt(1)
	v_mfma_f32_16x16x32_f16 v[36:39], v[12:15], v[210:213], v[16:19]
	v_mfma_f32_16x16x32_f16 v[32:35], v[12:15], v[214:217], v[32:35]
	v_mfma_f32_16x16x32_f16 v[158:161], v[12:15], v[218:221], v[158:161]
	v_mfma_f32_16x16x32_f16 v[166:169], v[12:15], v[222:225], v[166:169]
	v_mfma_f32_16x16x32_f16 v[190:193], v[238:241], v[210:213], v[190:193]
	v_mfma_f32_16x16x32_f16 v[202:205], v[238:241], v[214:217], v[202:205]
	v_mfma_f32_16x16x32_f16 v[206:209], v[238:241], v[218:221], v[206:209]
	v_mfma_f32_16x16x32_f16 v[186:189], v[238:241], v[222:225], v[186:189]
	s_setprio 0
	s_waitcnt vmcnt(4)
	s_waitcnt lgkmcnt(0)
	s_barrier
	ds_read_b128 v[210:213], v131 offset:32768
	ds_read_b128 v[214:217], v131 offset:34816
	ds_read_b128 v[218:221], v131 offset:36864
	ds_read_b128 v[222:225], v131 offset:38912
	ds_read_b128 v[12:15], v129 offset:32768
	ds_read_b128 v[16:19], v129 offset:34816
	s_add_u32 s70, s22, 0xa00
	v_lshl_add_u64 v[92:93], s[42:43], 0, v[196:197]
	s_addc_u32 s71, s90, 0
	s_mov_b32 m0, s1
	v_cvt_pk_f16_f32 v3, v2, v3
	global_load_lds_dwordx4 v[92:93], off
	v_cvt_pk_f16_f32 v2, v0, v1
	ds_write_b64 v100, v[2:3]
	global_load_dwordx4 v[0:3], v201, s[70:71] nt
	s_setprio 1
	s_waitcnt lgkmcnt(1)
	v_mfma_f32_16x16x32_f16 v[104:107], v[12:15], v[218:221], v[104:107]
	v_mfma_f32_16x16x32_f16 v[108:111], v[16:19], v[210:213], v[108:111]
	v_mfma_f32_16x16x32_f16 v[112:115], v[16:19], v[214:217], v[112:115]
	v_mfma_f32_16x16x32_f16 v[116:119], v[16:19], v[218:221], v[116:119]
	v_mfma_f32_16x16x32_f16 v[238:241], v[12:15], v[210:213], v[20:23]
	v_mfma_f32_16x16x32_f16 v[230:233], v[12:15], v[214:217], v[230:233]
	v_mfma_f32_16x16x32_f16 v[234:237], v[12:15], v[222:225], v[234:237]
	v_mfma_f32_16x16x32_f16 v[226:229], v[16:19], v[222:225], v[226:229]
	s_setprio 0
	ds_read_b128 v[16:19], v129 offset:36864
	ds_read_b128 v[20:23], v129 offset:38912
	s_mov_b32 m0, s92
	v_lshl_add_u64 v[12:13], v[92:93], 0, s[58:59]
	global_load_lds_dwordx4 v[12:13], off
	v_cvt_pk_f16_f32 v13, v66, v67
	v_cvt_pk_f16_f32 v12, v64, v65
	ds_write_b64 v100, v[12:13] offset:4096
	s_add_u32 s0, s22, 0x20a00
	s_addc_u32 s1, s90, 0
	global_load_dwordx4 v[12:15], v201, s[0:1] nt
	s_setprio 1
	s_waitcnt lgkmcnt(1)
	v_mfma_f32_16x16x32_f16 v[64:67], v[16:19], v[210:213], v[24:27]
	v_mfma_f32_16x16x32_f16 v[120:123], v[16:19], v[222:225], v[120:123]
	v_mfma_f32_16x16x32_f16 v[124:127], v[20:23], v[210:213], v[124:127]
	v_mfma_f32_16x16x32_f16 v[146:149], v[20:23], v[214:217], v[146:149]
	v_mfma_f32_16x16x32_f16 v[134:137], v[20:23], v[222:225], v[134:137]
	v_mfma_f32_16x16x32_f16 v[138:141], v[16:19], v[214:217], v[138:141]
	v_mfma_f32_16x16x32_f16 v[142:145], v[16:19], v[218:221], v[142:145]
	v_mfma_f32_16x16x32_f16 v[150:153], v[20:23], v[218:221], v[150:153]
	s_setprio 0
	ds_read_b128 v[20:23], v129 offset:40960
	ds_read_b128 v[24:27], v129 offset:43008
	s_mov_b32 m0, s91
	v_lshl_add_u64 v[16:17], v[92:93], 0, s[60:61]
	global_load_lds_dwordx4 v[16:17], off
	v_cvt_pk_f16_f32 v17, v70, v71
	v_cvt_pk_f16_f32 v16, v68, v69
	ds_write_b64 v100, v[16:17] offset:8192
	s_add_u32 s0, s22, 0x40a00
	s_addc_u32 s1, s90, 0
	global_load_dwordx4 v[16:19], v201, s[0:1] nt
	s_setprio 1
	s_waitcnt lgkmcnt(1)
	v_mfma_f32_16x16x32_f16 v[68:71], v[20:23], v[210:213], v[246:249]
	v_mfma_f32_16x16x32_f16 v[242:245], v[20:23], v[214:217], v[28:31]
	v_mfma_f32_16x16x32_f16 v[170:173], v[20:23], v[218:221], v[170:173]
	v_mfma_f32_16x16x32_f16 v[162:165], v[20:23], v[222:225], v[162:165]
	v_mfma_f32_16x16x32_f16 v[174:177], v[24:27], v[210:213], v[174:177]
	v_mfma_f32_16x16x32_f16 v[178:181], v[24:27], v[214:217], v[178:181]
	v_mfma_f32_16x16x32_f16 v[182:185], v[24:27], v[218:221], v[182:185]
	v_mfma_f32_16x16x32_f16 v[154:157], v[24:27], v[222:225], v[154:157]
	s_setprio 0
	ds_read_b128 v[24:27], v129 offset:45056
	ds_read_b128 v[28:31], v129 offset:47104
	s_mov_b32 m0, s73
	v_lshl_add_u64 v[20:21], v[92:93], 0, s[62:63]
	global_load_lds_dwordx4 v[20:21], off
	v_cvt_pk_f16_f32 v21, v74, v75
	v_cvt_pk_f16_f32 v20, v72, v73
	ds_write_b64 v100, v[20:21] offset:12288
	s_add_u32 s0, s22, 0x60a00
	s_addc_u32 s1, s90, 0
	global_load_dwordx4 v[20:23], v201, s[0:1] nt
	s_setprio 1
	s_waitcnt lgkmcnt(1)
	v_mfma_f32_16x16x32_f16 v[72:75], v[24:27], v[210:213], v[36:39]
	v_mfma_f32_16x16x32_f16 v[246:249], v[24:27], v[214:217], v[32:35]
	v_mfma_f32_16x16x32_f16 v[158:161], v[24:27], v[218:221], v[158:161]
	v_mfma_f32_16x16x32_f16 v[166:169], v[24:27], v[222:225], v[166:169]
	v_mfma_f32_16x16x32_f16 v[190:193], v[28:31], v[210:213], v[190:193]
	v_mfma_f32_16x16x32_f16 v[202:205], v[28:31], v[214:217], v[202:205]
	v_mfma_f32_16x16x32_f16 v[206:209], v[28:31], v[218:221], v[206:209]
	v_mfma_f32_16x16x32_f16 v[186:189], v[28:31], v[222:225], v[186:189]
	s_setprio 0
	ds_read_b128 v[210:213], v128 offset:32768
	ds_read_b128 v[214:217], v128 offset:34816
	ds_read_b128 v[218:221], v128 offset:36864
	ds_read_b128 v[222:225], v128 offset:38912
	ds_read_b128 v[28:31], v130 offset:32768
	ds_read_b128 v[32:35], v130 offset:34816
	v_cvt_pk_f16_f32 v25, v78, v79
	v_cvt_pk_f16_f32 v24, v76, v77
	ds_write_b64 v100, v[24:25] offset:16384
	s_add_u32 s0, s22, 0x80a00
	s_addc_u32 s1, s90, 0
	global_load_dwordx4 v[24:27], v201, s[0:1] nt
	s_setprio 1
	s_waitcnt lgkmcnt(1)
	v_mfma_f32_16x16x32_f16 v[76:79], v[28:31], v[210:213], v[238:241]
	v_mfma_f32_16x16x32_f16 v[104:107], v[28:31], v[218:221], v[104:107]
	v_mfma_f32_16x16x32_f16 v[108:111], v[32:35], v[210:213], v[108:111]
	v_mfma_f32_16x16x32_f16 v[112:115], v[32:35], v[214:217], v[112:115]
	v_mfma_f32_16x16x32_f16 v[116:119], v[32:35], v[218:221], v[116:119]
	v_mfma_f32_16x16x32_f16 v[230:233], v[28:31], v[214:217], v[230:233]
	v_mfma_f32_16x16x32_f16 v[234:237], v[28:31], v[222:225], v[234:237]
	v_mfma_f32_16x16x32_f16 v[226:229], v[32:35], v[222:225], v[226:229]
	s_setprio 0
	ds_read_b128 v[32:35], v130 offset:36864
	ds_read_b128 v[36:39], v130 offset:38912
	v_cvt_pk_f16_f32 v29, v82, v83
	v_cvt_pk_f16_f32 v28, v80, v81
	ds_write_b64 v100, v[28:29] offset:20480
	s_add_u32 s0, s22, 0xa0a00
	s_addc_u32 s1, s90, 0
	global_load_dwordx4 v[28:31], v201, s[0:1] nt
	s_setprio 1
	s_waitcnt lgkmcnt(1)
	v_mfma_f32_16x16x32_f16 v[80:83], v[32:35], v[210:213], v[64:67]
	v_mfma_f32_16x16x32_f16 v[120:123], v[32:35], v[222:225], v[120:123]
	v_mfma_f32_16x16x32_f16 v[124:127], v[36:39], v[210:213], v[124:127]
	v_mfma_f32_16x16x32_f16 v[146:149], v[36:39], v[214:217], v[146:149]
	v_mfma_f32_16x16x32_f16 v[134:137], v[36:39], v[222:225], v[134:137]
	v_mfma_f32_16x16x32_f16 v[138:141], v[32:35], v[214:217], v[138:141]
	v_mfma_f32_16x16x32_f16 v[142:145], v[32:35], v[218:221], v[142:145]
	v_mfma_f32_16x16x32_f16 v[150:153], v[36:39], v[218:221], v[150:153]
	s_setprio 0
	ds_read_b128 v[36:39], v130 offset:40960
	ds_read_b128 v[64:67], v130 offset:43008
	v_cvt_pk_f16_f32 v33, v86, v87
	v_cvt_pk_f16_f32 v32, v84, v85
	ds_write_b64 v100, v[32:33] offset:24576
	s_add_u32 s0, s22, 0xc0a00
	s_addc_u32 s1, s90, 0
	global_load_dwordx4 v[32:35], v201, s[0:1] nt
	s_setprio 1
	s_waitcnt lgkmcnt(1)
	v_mfma_f32_16x16x32_f16 v[68:71], v[36:39], v[210:213], v[68:71]
	v_mfma_f32_16x16x32_f16 v[84:87], v[36:39], v[214:217], v[242:245]
	v_mfma_f32_16x16x32_f16 v[170:173], v[36:39], v[218:221], v[170:173]
	v_mfma_f32_16x16x32_f16 v[162:165], v[36:39], v[222:225], v[162:165]
	v_mfma_f32_16x16x32_f16 v[174:177], v[64:67], v[210:213], v[174:177]
	v_mfma_f32_16x16x32_f16 v[178:181], v[64:67], v[214:217], v[178:181]
	v_mfma_f32_16x16x32_f16 v[182:185], v[64:67], v[218:221], v[182:185]
	v_mfma_f32_16x16x32_f16 v[154:157], v[64:67], v[222:225], v[154:157]
	s_setprio 0
	ds_read_b128 v[64:67], v130 offset:45056
	ds_read_b128 v[238:241], v130 offset:47104
	v_cvt_pk_f16_f32 v37, v90, v91
	v_cvt_pk_f16_f32 v36, v88, v89
	ds_write_b64 v100, v[36:37] offset:28672
	s_add_u32 s0, s22, 0xe0a00
	s_addc_u32 s1, s90, 0
	global_load_dwordx4 v[36:39], v201, s[0:1] nt
	s_setprio 1
	s_waitcnt lgkmcnt(1)
	v_mfma_f32_16x16x32_f16 v[72:75], v[64:67], v[210:213], v[72:75]
	v_mfma_f32_16x16x32_f16 v[88:91], v[64:67], v[214:217], v[246:249]
	v_mfma_f32_16x16x32_f16 v[158:161], v[64:67], v[218:221], v[158:161]
	v_mfma_f32_16x16x32_f16 v[166:169], v[64:67], v[222:225], v[166:169]
	v_mfma_f32_16x16x32_f16 v[190:193], v[238:241], v[210:213], v[190:193]
	v_mfma_f32_16x16x32_f16 v[202:205], v[238:241], v[214:217], v[202:205]
	v_mfma_f32_16x16x32_f16 v[206:209], v[238:241], v[218:221], v[206:209]
	v_mfma_f32_16x16x32_f16 v[186:189], v[238:241], v[222:225], v[186:189]
	s_setprio 0
	s_waitcnt vmcnt(4)
	s_waitcnt lgkmcnt(0)
	s_barrier
	ds_read_b128 v[210:213], v131
	ds_read_b128 v[214:217], v131 offset:2048
	ds_read_b128 v[218:221], v131 offset:4096
	ds_read_b128 v[222:225], v131 offset:6144
	ds_read_b128 v[64:67], v129
	ds_read_b128 v[238:241], v129 offset:2048
	s_add_u32 s70, s22, 0xb00
	v_lshl_add_u64 v[92:93], s[44:45], 0, v[196:197]
	s_addc_u32 s71, s90, 0
	v_readfirstlane_b32 s0, v95
	s_mov_b32 m0, s0
	v_cvt_pk_f16_f32 v7, v6, v7
	global_load_lds_dwordx4 v[92:93], off
	v_cvt_pk_f16_f32 v6, v4, v5
	ds_write_b64 v100, v[6:7] offset:32768
	global_load_dwordx4 v[4:7], v201, s[70:71] nt
	s_setprio 1
	s_waitcnt lgkmcnt(1)
	v_mfma_f32_16x16x32_f16 v[76:79], v[64:67], v[210:213], v[76:79]
	v_mfma_f32_16x16x32_f16 v[104:107], v[64:67], v[218:221], v[104:107]
	v_mfma_f32_16x16x32_f16 v[108:111], v[238:241], v[210:213], v[108:111]
	v_mfma_f32_16x16x32_f16 v[112:115], v[238:241], v[214:217], v[112:115]
	v_mfma_f32_16x16x32_f16 v[116:119], v[238:241], v[218:221], v[116:119]
	v_mfma_f32_16x16x32_f16 v[230:233], v[64:67], v[214:217], v[230:233]
	v_mfma_f32_16x16x32_f16 v[234:237], v[64:67], v[222:225], v[234:237]
	v_mfma_f32_16x16x32_f16 v[226:229], v[238:241], v[222:225], v[226:229]
	s_setprio 0
	ds_read_b128 v[238:241], v129 offset:4096
	ds_read_b128 v[242:245], v129 offset:6144
	v_readfirstlane_b32 s72, v96
	v_lshl_add_u64 v[64:65], v[92:93], 0, s[58:59]
	s_mov_b32 m0, s72
	v_cvt_pk_f16_f32 v11, v10, v11
	global_load_lds_dwordx4 v[64:65], off
	v_cvt_pk_f16_f32 v10, v8, v9
	ds_write_b64 v100, v[10:11] offset:36864
	s_add_u32 s70, s22, 0x20b00
	s_addc_u32 s71, s90, 0
	global_load_dwordx4 v[64:67], v201, s[70:71] nt
	s_setprio 1
	s_waitcnt lgkmcnt(1)
	v_mfma_f32_16x16x32_f16 v[8:11], v[238:241], v[210:213], v[80:83]
	v_mfma_f32_16x16x32_f16 v[80:83], v[238:241], v[214:217], v[138:141]
	v_mfma_f32_16x16x32_f16 v[138:141], v[238:241], v[218:221], v[142:145]
	v_mfma_f32_16x16x32_f16 v[120:123], v[238:241], v[222:225], v[120:123]
	v_mfma_f32_16x16x32_f16 v[124:127], v[242:245], v[210:213], v[124:127]
	v_mfma_f32_16x16x32_f16 v[142:145], v[242:245], v[214:217], v[146:149]
	v_mfma_f32_16x16x32_f16 v[146:149], v[242:245], v[218:221], v[150:153]
	v_mfma_f32_16x16x32_f16 v[134:137], v[242:245], v[222:225], v[134:137]
	s_setprio 0
	s_nop 0
	ds_read_b128 v[150:153], v129 offset:8192
	ds_read_b128 v[238:241], v129 offset:10240
	v_readfirstlane_b32 s71, v97
	v_lshl_add_u64 v[198:199], v[92:93], 0, s[60:61]
	s_mov_b32 m0, s71
	v_cvt_pk_f16_f32 v43, v42, v43
	global_load_lds_dwordx4 v[198:199], off
	v_cvt_pk_f16_f32 v42, v40, v41
	ds_write_b64 v100, v[42:43] offset:40960
	s_add_u32 s80, s22, 0x40b00
	s_addc_u32 s81, s90, 0
	global_load_dwordx4 v[40:43], v201, s[80:81] nt
	s_setprio 1
	s_waitcnt lgkmcnt(1)
	v_mfma_f32_16x16x32_f16 v[68:71], v[150:153], v[210:213], v[68:71]
	v_mfma_f32_16x16x32_f16 v[84:87], v[150:153], v[214:217], v[84:87]
	v_mfma_f32_16x16x32_f16 v[170:173], v[150:153], v[218:221], v[170:173]
	v_mfma_f32_16x16x32_f16 v[150:153], v[150:153], v[222:225], v[162:165]
	v_mfma_f32_16x16x32_f16 v[162:165], v[238:241], v[210:213], v[174:177]
	v_mfma_f32_16x16x32_f16 v[174:177], v[238:241], v[214:217], v[178:181]
	v_mfma_f32_16x16x32_f16 v[178:181], v[238:241], v[218:221], v[182:185]
	v_mfma_f32_16x16x32_f16 v[154:157], v[238:241], v[222:225], v[154:157]
	s_setprio 0
	s_nop 0
	ds_read_b128 v[182:185], v129 offset:12288
	ds_read_b128 v[238:241], v129 offset:14336
	v_readfirstlane_b32 s70, v98
	v_lshl_add_u64 v[92:93], v[92:93], 0, s[62:63]
	s_mov_b32 m0, s70
	v_cvt_pk_f16_f32 v47, v46, v47
	global_load_lds_dwordx4 v[92:93], off
	v_cvt_pk_f16_f32 v46, v44, v45
	ds_write_b64 v100, v[46:47] offset:45056
	s_add_u32 s80, s22, 0x60b00
	s_addc_u32 s81, s90, 0
	global_load_dwordx4 v[44:47], v201, s[80:81] nt
	s_setprio 1
	s_waitcnt lgkmcnt(1)
	v_mfma_f32_16x16x32_f16 v[72:75], v[182:185], v[210:213], v[72:75]
	v_mfma_f32_16x16x32_f16 v[88:91], v[182:185], v[214:217], v[88:91]
	v_mfma_f32_16x16x32_f16 v[158:161], v[182:185], v[218:221], v[158:161]
	v_mfma_f32_16x16x32_f16 v[166:169], v[182:185], v[222:225], v[166:169]
	v_mfma_f32_16x16x32_f16 v[182:185], v[238:241], v[210:213], v[190:193]
	v_mfma_f32_16x16x32_f16 v[190:193], v[238:241], v[214:217], v[202:205]
	v_mfma_f32_16x16x32_f16 v[202:205], v[238:241], v[218:221], v[206:209]
	v_mfma_f32_16x16x32_f16 v[186:189], v[238:241], v[222:225], v[186:189]
	s_setprio 0
	s_nop 0
	ds_read_b128 v[206:209], v128
	ds_read_b128 v[210:213], v128 offset:2048
	ds_read_b128 v[214:217], v128 offset:4096
	ds_read_b128 v[218:221], v128 offset:6144
	ds_read_b128 v[222:225], v130
	ds_read_b128 v[238:241], v130 offset:2048
	v_cvt_pk_f16_f32 v51, v50, v51
	v_cvt_pk_f16_f32 v50, v48, v49
	ds_write_b64 v100, v[50:51] offset:49152
	s_add_u32 s80, s22, 0x80b00
	s_addc_u32 s81, s90, 0
	global_load_dwordx4 v[48:51], v201, s[80:81] nt
	s_setprio 1
	s_waitcnt lgkmcnt(1)
	v_mfma_f32_16x16x32_f16 v[76:79], v[222:225], v[206:209], v[76:79]
	v_mfma_f32_16x16x32_f16 v[104:107], v[222:225], v[214:217], v[104:107]
	v_mfma_f32_16x16x32_f16 v[108:111], v[238:241], v[206:209], v[108:111]
	v_mfma_f32_16x16x32_f16 v[112:115], v[238:241], v[210:213], v[112:115]
	v_mfma_f32_16x16x32_f16 v[116:119], v[238:241], v[214:217], v[116:119]
	v_mfma_f32_16x16x32_f16 v[230:233], v[222:225], v[210:213], v[230:233]
	v_mfma_f32_16x16x32_f16 v[222:225], v[222:225], v[218:221], v[234:237]
	v_mfma_f32_16x16x32_f16 v[226:229], v[238:241], v[218:221], v[226:229]
	s_setprio 0
	s_nop 0
	ds_read_b128 v[234:237], v130 offset:4096
	ds_read_b128 v[238:241], v130 offset:6144
	v_cvt_pk_f16_f32 v55, v54, v55
	v_cvt_pk_f16_f32 v54, v52, v53
	ds_write_b64 v100, v[54:55] offset:53248
	s_add_u32 s80, s22, 0xa0b00
	s_addc_u32 s81, s90, 0
	global_load_dwordx4 v[52:55], v201, s[80:81] nt
	s_setprio 1
	s_waitcnt lgkmcnt(1)
	v_mfma_f32_16x16x32_f16 v[80:83], v[234:237], v[210:213], v[80:83]
	v_mfma_f32_16x16x32_f16 v[120:123], v[234:237], v[218:221], v[120:123]
	v_mfma_f32_16x16x32_f16 v[124:127], v[238:241], v[206:209], v[124:127]
	v_mfma_f32_16x16x32_f16 v[146:149], v[238:241], v[214:217], v[146:149]
	v_mfma_f32_16x16x32_f16 v[134:137], v[238:241], v[218:221], v[134:137]
	v_mfma_f32_16x16x32_f16 v[242:245], v[234:237], v[206:209], v[8:11]
	v_mfma_f32_16x16x32_f16 v[138:141], v[234:237], v[214:217], v[138:141]
	v_mfma_f32_16x16x32_f16 v[142:145], v[238:241], v[210:213], v[142:145]
	s_setprio 0
	ds_read_b128 v[8:11], v130 offset:8192
	ds_read_b128 v[234:237], v130 offset:10240
	v_cvt_pk_f16_f32 v59, v58, v59
	v_cvt_pk_f16_f32 v58, v56, v57
	ds_write_b64 v100, v[58:59] offset:57344
	s_add_u32 s80, s22, 0xc0b00
	s_addc_u32 s81, s90, 0
	global_load_dwordx4 v[56:59], v201, s[80:81] nt
	s_setprio 1
	s_waitcnt lgkmcnt(1)
	v_mfma_f32_16x16x32_f16 v[84:87], v[8:11], v[210:213], v[84:87]
	v_mfma_f32_16x16x32_f16 v[238:241], v[8:11], v[206:209], v[68:71]
	v_mfma_f32_16x16x32_f16 v[170:173], v[8:11], v[214:217], v[170:173]
	v_mfma_f32_16x16x32_f16 v[150:153], v[8:11], v[218:221], v[150:153]
	v_mfma_f32_16x16x32_f16 v[162:165], v[234:237], v[206:209], v[162:165]
	v_mfma_f32_16x16x32_f16 v[174:177], v[234:237], v[210:213], v[174:177]
	v_mfma_f32_16x16x32_f16 v[178:181], v[234:237], v[214:217], v[178:181]
	v_mfma_f32_16x16x32_f16 v[154:157], v[234:237], v[218:221], v[154:157]
	s_setprio 0
	ds_read_b128 v[8:11], v130 offset:12288
	ds_read_b128 v[68:71], v130 offset:14336
	v_cvt_pk_f16_f32 v63, v62, v63
	v_cvt_pk_f16_f32 v62, v60, v61
	ds_write_b64 v100, v[62:63] offset:61440
	s_add_u32 s80, s22, 0xe0b00
	s_addc_u32 s81, s90, 0
	global_load_dwordx4 v[60:63], v201, s[80:81] nt
	s_setprio 1
	s_waitcnt lgkmcnt(1)
	v_mfma_f32_16x16x32_f16 v[88:91], v[8:11], v[210:213], v[88:91]
	v_mfma_f32_16x16x32_f16 v[234:237], v[8:11], v[206:209], v[72:75]
	v_mfma_f32_16x16x32_f16 v[158:161], v[8:11], v[214:217], v[158:161]
	v_mfma_f32_16x16x32_f16 v[166:169], v[8:11], v[218:221], v[166:169]
	v_mfma_f32_16x16x32_f16 v[182:185], v[68:71], v[206:209], v[182:185]
	v_mfma_f32_16x16x32_f16 v[190:193], v[68:71], v[210:213], v[190:193]
	v_mfma_f32_16x16x32_f16 v[202:205], v[68:71], v[214:217], v[202:205]
	v_mfma_f32_16x16x32_f16 v[186:189], v[68:71], v[218:221], v[186:189]
	s_setprio 0
	s_waitcnt vmcnt(4)
	s_waitcnt lgkmcnt(0)
	s_barrier
	ds_read_b128 v[206:209], v131 offset:32768
	ds_read_b128 v[210:213], v131 offset:34816
	ds_read_b128 v[214:217], v131 offset:36864
	ds_read_b128 v[218:221], v131 offset:38912
	ds_read_b128 v[68:71], v129 offset:32768
	ds_read_b128 v[72:75], v129 offset:34816
	s_add_u32 s80, s22, 0xc00
	v_lshl_add_u64 v[92:93], s[46:47], 0, v[196:197]
	s_addc_u32 s81, s90, 0
	v_readfirstlane_b32 s1, v94
	s_mov_b32 m0, s1
	v_cvt_pk_f16_f32 v3, v2, v3
	global_load_lds_dwordx4 v[92:93], off
	v_cvt_pk_f16_f32 v2, v0, v1
	ds_write_b64 v100, v[2:3]
	global_load_dwordx4 v[8:11], v201, s[80:81] nt
	s_setprio 1
	s_waitcnt lgkmcnt(1)
	v_mfma_f32_16x16x32_f16 v[0:3], v[68:71], v[206:209], v[76:79]
	v_mfma_f32_16x16x32_f16 v[104:107], v[68:71], v[214:217], v[104:107]
	v_mfma_f32_16x16x32_f16 v[108:111], v[72:75], v[206:209], v[108:111]
	v_mfma_f32_16x16x32_f16 v[112:115], v[72:75], v[210:213], v[112:115]
	v_mfma_f32_16x16x32_f16 v[116:119], v[72:75], v[214:217], v[116:119]
	v_mfma_f32_16x16x32_f16 v[230:233], v[68:71], v[210:213], v[230:233]
	v_mfma_f32_16x16x32_f16 v[222:225], v[68:71], v[218:221], v[222:225]
	v_mfma_f32_16x16x32_f16 v[226:229], v[72:75], v[218:221], v[226:229]
	s_setprio 0
	ds_read_b128 v[72:75], v129 offset:36864
	ds_read_b128 v[76:79], v129 offset:38912
	v_readfirstlane_b32 s92, v99
	v_lshl_add_u64 v[68:69], v[92:93], 0, s[58:59]
	s_mov_b32 m0, s92
	v_cvt_pk_f16_f32 v15, v14, v15
	global_load_lds_dwordx4 v[68:69], off
	v_cvt_pk_f16_f32 v14, v12, v13
	ds_write_b64 v100, v[14:15] offset:4096
	s_add_u32 s80, s22, 0x20c00
	s_addc_u32 s81, s90, 0
	global_load_dwordx4 v[68:71], v201, s[80:81] nt
	s_setprio 1
	s_waitcnt lgkmcnt(1)
	v_mfma_f32_16x16x32_f16 v[12:15], v[72:75], v[206:209], v[242:245]
	v_mfma_f32_16x16x32_f16 v[120:123], v[72:75], v[218:221], v[120:123]
	v_mfma_f32_16x16x32_f16 v[124:127], v[76:79], v[206:209], v[124:127]
	v_mfma_f32_16x16x32_f16 v[146:149], v[76:79], v[214:217], v[146:149]
	v_mfma_f32_16x16x32_f16 v[134:137], v[76:79], v[218:221], v[134:137]
	v_mfma_f32_16x16x32_f16 v[242:245], v[72:75], v[210:213], v[80:83]
	v_mfma_f32_16x16x32_f16 v[138:141], v[72:75], v[214:217], v[138:141]
	v_mfma_f32_16x16x32_f16 v[142:145], v[76:79], v[210:213], v[142:145]
	s_setprio 0
	ds_read_b128 v[76:79], v129 offset:40960
	ds_read_b128 v[80:83], v129 offset:43008
	v_readfirstlane_b32 s91, v101
	v_lshl_add_u64 v[72:73], v[92:93], 0, s[60:61]
	s_mov_b32 m0, s91
	v_cvt_pk_f16_f32 v19, v18, v19
	global_load_lds_dwordx4 v[72:73], off
	v_cvt_pk_f16_f32 v18, v16, v17
	ds_write_b64 v100, v[18:19] offset:8192
	s_add_u32 s80, s22, 0x40c00
	s_addc_u32 s81, s90, 0
	global_load_dwordx4 v[72:75], v201, s[80:81] nt
	s_setprio 1
	s_waitcnt lgkmcnt(1)
	v_mfma_f32_16x16x32_f16 v[16:19], v[76:79], v[206:209], v[238:241]
	v_mfma_f32_16x16x32_f16 v[238:241], v[76:79], v[210:213], v[84:87]
	v_mfma_f32_16x16x32_f16 v[170:173], v[76:79], v[214:217], v[170:173]
	v_mfma_f32_16x16x32_f16 v[150:153], v[76:79], v[218:221], v[150:153]
	v_mfma_f32_16x16x32_f16 v[162:165], v[80:83], v[206:209], v[162:165]
	v_mfma_f32_16x16x32_f16 v[174:177], v[80:83], v[210:213], v[174:177]
	v_mfma_f32_16x16x32_f16 v[178:181], v[80:83], v[214:217], v[178:181]
	v_mfma_f32_16x16x32_f16 v[154:157], v[80:83], v[218:221], v[154:157]
	s_setprio 0
	ds_read_b128 v[80:83], v129 offset:45056
	ds_read_b128 v[84:87], v129 offset:47104
	v_readfirstlane_b32 s73, v102
	v_lshl_add_u64 v[76:77], v[92:93], 0, s[62:63]
	s_mov_b32 m0, s73
	v_cvt_pk_f16_f32 v23, v22, v23
	global_load_lds_dwordx4 v[76:77], off
	v_cvt_pk_f16_f32 v22, v20, v21
	ds_write_b64 v100, v[22:23] offset:12288
	s_add_u32 s80, s22, 0x60c00
	s_addc_u32 s81, s90, 0
	global_load_dwordx4 v[76:79], v201, s[80:81] nt
	s_setprio 1
	s_waitcnt lgkmcnt(1)
	v_mfma_f32_16x16x32_f16 v[20:23], v[80:83], v[206:209], v[234:237]
	v_mfma_f32_16x16x32_f16 v[234:237], v[80:83], v[210:213], v[88:91]
	v_mfma_f32_16x16x32_f16 v[158:161], v[80:83], v[214:217], v[158:161]
	v_mfma_f32_16x16x32_f16 v[166:169], v[80:83], v[218:221], v[166:169]
	v_mfma_f32_16x16x32_f16 v[182:185], v[84:87], v[206:209], v[182:185]
	v_mfma_f32_16x16x32_f16 v[190:193], v[84:87], v[210:213], v[190:193]
	v_mfma_f32_16x16x32_f16 v[202:205], v[84:87], v[214:217], v[202:205]
	v_mfma_f32_16x16x32_f16 v[186:189], v[84:87], v[218:221], v[186:189]
	s_setprio 0
	ds_read_b128 v[206:209], v128 offset:32768
	ds_read_b128 v[210:213], v128 offset:34816
	ds_read_b128 v[214:217], v128 offset:36864
	ds_read_b128 v[218:221], v128 offset:38912
	ds_read_b128 v[84:87], v130 offset:32768
	ds_read_b128 v[88:91], v130 offset:34816
	v_cvt_pk_f16_f32 v27, v26, v27
	v_cvt_pk_f16_f32 v26, v24, v25
	ds_write_b64 v100, v[26:27] offset:16384
	s_add_u32 s80, s22, 0x80c00
	s_addc_u32 s81, s90, 0
	global_load_dwordx4 v[80:83], v201, s[80:81] nt
	s_setprio 1
	s_waitcnt lgkmcnt(1)
	v_mfma_f32_16x16x32_f16 v[24:27], v[84:87], v[206:209], v[0:3]
	v_mfma_f32_16x16x32_f16 v[104:107], v[84:87], v[214:217], v[104:107]
	v_mfma_f32_16x16x32_f16 v[108:111], v[88:91], v[206:209], v[108:111]
	v_mfma_f32_16x16x32_f16 v[112:115], v[88:91], v[210:213], v[112:115]
	v_mfma_f32_16x16x32_f16 v[116:119], v[88:91], v[214:217], v[116:119]
	v_mfma_f32_16x16x32_f16 v[230:233], v[84:87], v[210:213], v[230:233]
	v_mfma_f32_16x16x32_f16 v[222:225], v[84:87], v[218:221], v[222:225]
	v_mfma_f32_16x16x32_f16 v[226:229], v[88:91], v[218:221], v[226:229]
	s_setprio 0
	ds_read_b128 v[0:3], v130 offset:36864
	ds_read_b128 v[88:91], v130 offset:38912
	v_cvt_pk_f16_f32 v31, v30, v31
	v_cvt_pk_f16_f32 v30, v28, v29
	ds_write_b64 v100, v[30:31] offset:20480
	s_add_u32 s80, s22, 0xa0c00
	s_addc_u32 s81, s90, 0
	global_load_dwordx4 v[84:87], v201, s[80:81] nt
	s_setprio 1
	s_waitcnt lgkmcnt(1)
	v_mfma_f32_16x16x32_f16 v[12:15], v[0:3], v[206:209], v[12:15]
	v_mfma_f32_16x16x32_f16 v[28:31], v[0:3], v[210:213], v[242:245]
	v_mfma_f32_16x16x32_f16 v[120:123], v[0:3], v[218:221], v[120:123]
	v_mfma_f32_16x16x32_f16 v[124:127], v[88:91], v[206:209], v[124:127]
	v_mfma_f32_16x16x32_f16 v[146:149], v[88:91], v[214:217], v[146:149]
	v_mfma_f32_16x16x32_f16 v[134:137], v[88:91], v[218:221], v[134:137]
	v_mfma_f32_16x16x32_f16 v[138:141], v[0:3], v[214:217], v[138:141]
	v_mfma_f32_16x16x32_f16 v[142:145], v[88:91], v[210:213], v[142:145]
	s_setprio 0
	ds_read_b128 v[0:3], v130 offset:40960
	ds_read_b128 v[242:245], v130 offset:43008
	v_cvt_pk_f16_f32 v35, v34, v35
	v_cvt_pk_f16_f32 v34, v32, v33
	ds_write_b64 v100, v[34:35] offset:24576
	s_add_u32 s80, s22, 0xc0c00
	s_addc_u32 s81, s90, 0
	global_load_dwordx4 v[88:91], v201, s[80:81] nt
	s_setprio 1
	s_waitcnt lgkmcnt(1)
	v_mfma_f32_16x16x32_f16 v[16:19], v[0:3], v[206:209], v[16:19]
	v_mfma_f32_16x16x32_f16 v[32:35], v[0:3], v[210:213], v[238:241]
	v_mfma_f32_16x16x32_f16 v[170:173], v[0:3], v[214:217], v[170:173]
	v_mfma_f32_16x16x32_f16 v[150:153], v[0:3], v[218:221], v[150:153]
	v_mfma_f32_16x16x32_f16 v[162:165], v[242:245], v[206:209], v[162:165]
	v_mfma_f32_16x16x32_f16 v[174:177], v[242:245], v[210:213], v[174:177]
	v_mfma_f32_16x16x32_f16 v[178:181], v[242:245], v[214:217], v[178:181]
	v_mfma_f32_16x16x32_f16 v[154:157], v[242:245], v[218:221], v[154:157]
	s_setprio 0
	ds_read_b128 v[0:3], v130 offset:45056
	ds_read_b128 v[238:241], v130 offset:47104
	v_cvt_pk_f16_f32 v39, v38, v39
	v_cvt_pk_f16_f32 v38, v36, v37
	ds_write_b64 v100, v[38:39] offset:28672
	s_add_u32 s80, s22, 0xe0c00
	s_addc_u32 s81, s90, 0
	global_load_dwordx4 v[36:39], v201, s[80:81] nt
	s_setprio 1
	s_waitcnt lgkmcnt(1)
	v_mfma_f32_16x16x32_f16 v[20:23], v[0:3], v[206:209], v[20:23]
	v_mfma_f32_16x16x32_f16 v[234:237], v[0:3], v[210:213], v[234:237]
	v_mfma_f32_16x16x32_f16 v[158:161], v[0:3], v[214:217], v[158:161]
	v_mfma_f32_16x16x32_f16 v[166:169], v[0:3], v[218:221], v[166:169]
	v_mfma_f32_16x16x32_f16 v[182:185], v[238:241], v[206:209], v[182:185]
	v_mfma_f32_16x16x32_f16 v[190:193], v[238:241], v[210:213], v[190:193]
	v_mfma_f32_16x16x32_f16 v[202:205], v[238:241], v[214:217], v[202:205]
	v_mfma_f32_16x16x32_f16 v[186:189], v[238:241], v[218:221], v[186:189]
	s_setprio 0
	s_waitcnt vmcnt(4)
	s_waitcnt lgkmcnt(0)
	s_barrier
	ds_read_b128 v[206:209], v131
	ds_read_b128 v[210:213], v131 offset:2048
	ds_read_b128 v[214:217], v131 offset:4096
	ds_read_b128 v[218:221], v131 offset:6144
	ds_read_b128 v[238:241], v129
	ds_read_b128 v[242:245], v129 offset:2048
	s_add_u32 s80, s22, 0xd00
	v_lshl_add_u64 v[92:93], s[48:49], 0, v[196:197]
	s_addc_u32 s81, s90, 0
	s_mov_b32 m0, s0
	v_cvt_pk_f16_f32 v1, v6, v7
	global_load_lds_dwordx4 v[92:93], off
	v_cvt_pk_f16_f32 v0, v4, v5
	ds_write_b64 v100, v[0:1] offset:32768
	global_load_dwordx4 v[0:3], v201, s[80:81] nt
	s_setprio 1
	s_waitcnt lgkmcnt(1)
	v_mfma_f32_16x16x32_f16 v[24:27], v[238:241], v[206:209], v[24:27]
	v_mfma_f32_16x16x32_f16 v[104:107], v[238:241], v[214:217], v[104:107]
	v_mfma_f32_16x16x32_f16 v[108:111], v[242:245], v[206:209], v[108:111]
	v_mfma_f32_16x16x32_f16 v[112:115], v[242:245], v[210:213], v[112:115]
	v_mfma_f32_16x16x32_f16 v[116:119], v[242:245], v[214:217], v[116:119]
	v_mfma_f32_16x16x32_f16 v[230:233], v[238:241], v[210:213], v[230:233]
	v_mfma_f32_16x16x32_f16 v[222:225], v[238:241], v[218:221], v[222:225]
	v_mfma_f32_16x16x32_f16 v[226:229], v[242:245], v[218:221], v[226:229]
	s_setprio 0
	ds_read_b128 v[238:241], v129 offset:4096
	ds_read_b128 v[242:245], v129 offset:6144
	s_mov_b32 m0, s72
	v_lshl_add_u64 v[4:5], v[92:93], 0, s[58:59]
	global_load_lds_dwordx4 v[4:5], off
	v_cvt_pk_f16_f32 v5, v66, v67
	v_cvt_pk_f16_f32 v4, v64, v65
	ds_write_b64 v100, v[4:5] offset:36864
	s_add_u32 s80, s22, 0x20d00
	s_addc_u32 s81, s90, 0
	global_load_dwordx4 v[4:7], v201, s[80:81] nt
	s_setprio 1
	s_waitcnt lgkmcnt(1)
	v_mfma_f32_16x16x32_f16 v[64:67], v[238:241], v[206:209], v[12:15]
	v_mfma_f32_16x16x32_f16 v[28:31], v[238:241], v[210:213], v[28:31]
	v_mfma_f32_16x16x32_f16 v[120:123], v[238:241], v[218:221], v[120:123]
	v_mfma_f32_16x16x32_f16 v[124:127], v[242:245], v[206:209], v[124:127]
	v_mfma_f32_16x16x32_f16 v[146:149], v[242:245], v[214:217], v[146:149]
	v_mfma_f32_16x16x32_f16 v[134:137], v[242:245], v[218:221], v[134:137]
	v_mfma_f32_16x16x32_f16 v[138:141], v[238:241], v[214:217], v[138:141]
	v_mfma_f32_16x16x32_f16 v[142:145], v[242:245], v[210:213], v[142:145]
	s_setprio 0
	ds_read_b128 v[238:241], v129 offset:8192
	ds_read_b128 v[242:245], v129 offset:10240
	s_mov_b32 m0, s71
	v_lshl_add_u64 v[12:13], v[92:93], 0, s[60:61]
	global_load_lds_dwordx4 v[12:13], off
	v_cvt_pk_f16_f32 v13, v42, v43
	v_cvt_pk_f16_f32 v12, v40, v41
	ds_write_b64 v100, v[12:13] offset:40960
	s_add_u32 s80, s22, 0x40d00
	s_addc_u32 s81, s90, 0
	global_load_dwordx4 v[12:15], v201, s[80:81] nt
	s_setprio 1
	s_waitcnt lgkmcnt(1)
	v_mfma_f32_16x16x32_f16 v[40:43], v[238:241], v[206:209], v[16:19]
	v_mfma_f32_16x16x32_f16 v[32:35], v[238:241], v[210:213], v[32:35]
	v_mfma_f32_16x16x32_f16 v[170:173], v[238:241], v[214:217], v[170:173]
	v_mfma_f32_16x16x32_f16 v[150:153], v[238:241], v[218:221], v[150:153]
	v_mfma_f32_16x16x32_f16 v[162:165], v[242:245], v[206:209], v[162:165]
	v_mfma_f32_16x16x32_f16 v[174:177], v[242:245], v[210:213], v[174:177]
	v_mfma_f32_16x16x32_f16 v[178:181], v[242:245], v[214:217], v[178:181]
	v_mfma_f32_16x16x32_f16 v[154:157], v[242:245], v[218:221], v[154:157]
	s_setprio 0
	ds_read_b128 v[238:241], v129 offset:12288
	ds_read_b128 v[242:245], v129 offset:14336
	s_mov_b32 m0, s70
	v_lshl_add_u64 v[16:17], v[92:93], 0, s[62:63]
	global_load_lds_dwordx4 v[16:17], off
	v_cvt_pk_f16_f32 v17, v46, v47
	v_cvt_pk_f16_f32 v16, v44, v45
	ds_write_b64 v100, v[16:17] offset:45056
	s_add_u32 s70, s22, 0x60d00
	s_addc_u32 s71, s90, 0
	global_load_dwordx4 v[16:19], v201, s[70:71] nt
	s_setprio 1
	s_waitcnt lgkmcnt(1)
	v_mfma_f32_16x16x32_f16 v[44:47], v[238:241], v[206:209], v[20:23]
	v_mfma_f32_16x16x32_f16 v[234:237], v[238:241], v[210:213], v[234:237]
	v_mfma_f32_16x16x32_f16 v[158:161], v[238:241], v[214:217], v[158:161]
	v_mfma_f32_16x16x32_f16 v[166:169], v[238:241], v[218:221], v[166:169]
	v_mfma_f32_16x16x32_f16 v[182:185], v[242:245], v[206:209], v[182:185]
	v_mfma_f32_16x16x32_f16 v[190:193], v[242:245], v[210:213], v[190:193]
	v_mfma_f32_16x16x32_f16 v[202:205], v[242:245], v[214:217], v[202:205]
	v_mfma_f32_16x16x32_f16 v[186:189], v[242:245], v[218:221], v[186:189]
	s_setprio 0
	ds_read_b128 v[206:209], v128
	ds_read_b128 v[210:213], v128 offset:2048
	ds_read_b128 v[214:217], v128 offset:4096
	ds_read_b128 v[218:221], v128 offset:6144
	ds_read_b128 v[238:241], v130
	ds_read_b128 v[242:245], v130 offset:2048
	v_cvt_pk_f16_f32 v21, v50, v51
	v_cvt_pk_f16_f32 v20, v48, v49
	ds_write_b64 v100, v[20:21] offset:49152
	s_add_u32 s70, s22, 0x80d00
	s_addc_u32 s71, s90, 0
	global_load_dwordx4 v[20:23], v201, s[70:71] nt
	s_setprio 1
	s_waitcnt lgkmcnt(1)
	v_mfma_f32_16x16x32_f16 v[48:51], v[238:241], v[206:209], v[24:27]
	v_mfma_f32_16x16x32_f16 v[104:107], v[238:241], v[214:217], v[104:107]
	v_mfma_f32_16x16x32_f16 v[108:111], v[242:245], v[206:209], v[108:111]
	v_mfma_f32_16x16x32_f16 v[112:115], v[242:245], v[210:213], v[112:115]
	v_mfma_f32_16x16x32_f16 v[116:119], v[242:245], v[214:217], v[116:119]
	v_mfma_f32_16x16x32_f16 v[230:233], v[238:241], v[210:213], v[230:233]
	v_mfma_f32_16x16x32_f16 v[222:225], v[238:241], v[218:221], v[222:225]
	v_mfma_f32_16x16x32_f16 v[226:229], v[242:245], v[218:221], v[226:229]
	s_setprio 0
	ds_read_b128 v[238:241], v130 offset:4096
	ds_read_b128 v[242:245], v130 offset:6144
	v_cvt_pk_f16_f32 v25, v54, v55
	v_cvt_pk_f16_f32 v24, v52, v53
	ds_write_b64 v100, v[24:25] offset:53248
	s_add_u32 s70, s22, 0xa0d00
	s_addc_u32 s71, s90, 0
	global_load_dwordx4 v[24:27], v201, s[70:71] nt
	s_setprio 1
	s_waitcnt lgkmcnt(1)
	v_mfma_f32_16x16x32_f16 v[52:55], v[238:241], v[206:209], v[64:67]
	v_mfma_f32_16x16x32_f16 v[64:67], v[238:241], v[210:213], v[28:31]
	v_mfma_f32_16x16x32_f16 v[120:123], v[238:241], v[218:221], v[120:123]
	v_mfma_f32_16x16x32_f16 v[124:127], v[242:245], v[206:209], v[124:127]
	v_mfma_f32_16x16x32_f16 v[146:149], v[242:245], v[214:217], v[146:149]
	v_mfma_f32_16x16x32_f16 v[134:137], v[242:245], v[218:221], v[134:137]
	v_mfma_f32_16x16x32_f16 v[138:141], v[238:241], v[214:217], v[138:141]
	v_mfma_f32_16x16x32_f16 v[142:145], v[242:245], v[210:213], v[142:145]
	s_setprio 0
	ds_read_b128 v[238:241], v130 offset:8192
	ds_read_b128 v[242:245], v130 offset:10240
	v_cvt_pk_f16_f32 v29, v58, v59
	v_cvt_pk_f16_f32 v28, v56, v57
	ds_write_b64 v100, v[28:29] offset:57344
	s_add_u32 s70, s22, 0xc0d00
	s_addc_u32 s71, s90, 0
	global_load_dwordx4 v[28:31], v201, s[70:71] nt
	s_setprio 1
	s_waitcnt lgkmcnt(1)
	v_mfma_f32_16x16x32_f16 v[56:59], v[238:241], v[206:209], v[40:43]
	v_mfma_f32_16x16x32_f16 v[246:249], v[238:241], v[210:213], v[32:35]
	v_mfma_f32_16x16x32_f16 v[170:173], v[238:241], v[214:217], v[170:173]
	v_mfma_f32_16x16x32_f16 v[150:153], v[238:241], v[218:221], v[150:153]
	v_mfma_f32_16x16x32_f16 v[162:165], v[242:245], v[206:209], v[162:165]
	v_mfma_f32_16x16x32_f16 v[174:177], v[242:245], v[210:213], v[174:177]
	v_mfma_f32_16x16x32_f16 v[178:181], v[242:245], v[214:217], v[178:181]
	v_mfma_f32_16x16x32_f16 v[154:157], v[242:245], v[218:221], v[154:157]
	s_setprio 0
	ds_read_b128 v[40:43], v130 offset:12288
	ds_read_b128 v[238:241], v130 offset:14336
	v_cvt_pk_f16_f32 v33, v62, v63
	v_cvt_pk_f16_f32 v32, v60, v61
	ds_write_b64 v100, v[32:33] offset:61440
	s_add_u32 s70, s22, 0xe0d00
	s_addc_u32 s71, s90, 0
	global_load_dwordx4 v[32:35], v201, s[70:71] nt
	s_setprio 1
	s_waitcnt lgkmcnt(1)
	v_mfma_f32_16x16x32_f16 v[60:63], v[40:43], v[206:209], v[44:47]
	v_mfma_f32_16x16x32_f16 v[234:237], v[40:43], v[210:213], v[234:237]
	v_mfma_f32_16x16x32_f16 v[158:161], v[40:43], v[214:217], v[158:161]
	v_mfma_f32_16x16x32_f16 v[166:169], v[40:43], v[218:221], v[166:169]
	v_mfma_f32_16x16x32_f16 v[182:185], v[238:241], v[206:209], v[182:185]
	v_mfma_f32_16x16x32_f16 v[190:193], v[238:241], v[210:213], v[190:193]
	v_mfma_f32_16x16x32_f16 v[202:205], v[238:241], v[214:217], v[202:205]
	v_mfma_f32_16x16x32_f16 v[186:189], v[238:241], v[218:221], v[186:189]
	s_setprio 0
	s_waitcnt vmcnt(4)
	s_waitcnt lgkmcnt(0)
	s_barrier
	ds_read_b128 v[206:209], v131 offset:32768
	ds_read_b128 v[210:213], v131 offset:34816
	ds_read_b128 v[214:217], v131 offset:36864
	ds_read_b128 v[218:221], v131 offset:38912
	ds_read_b128 v[40:43], v129 offset:32768
	ds_read_b128 v[44:47], v129 offset:34816
	s_add_u32 s70, s22, 0xe00
	v_lshl_add_u64 v[92:93], s[50:51], 0, v[196:197]
	s_addc_u32 s71, s90, 0
	s_mov_b32 m0, s1
	v_cvt_pk_f16_f32 v11, v10, v11
	global_load_lds_dwordx4 v[92:93], off
	v_cvt_pk_f16_f32 v10, v8, v9
	ds_write_b64 v100, v[10:11]
	global_load_dwordx4 v[8:11], v201, s[70:71] nt
	s_setprio 1
	s_waitcnt lgkmcnt(1)
	v_mfma_f32_16x16x32_f16 v[104:107], v[40:43], v[214:217], v[104:107]
	v_mfma_f32_16x16x32_f16 v[108:111], v[44:47], v[206:209], v[108:111]
	v_mfma_f32_16x16x32_f16 v[112:115], v[44:47], v[210:213], v[112:115]
	v_mfma_f32_16x16x32_f16 v[116:119], v[44:47], v[214:217], v[116:119]
	v_mfma_f32_16x16x32_f16 v[238:241], v[40:43], v[206:209], v[48:51]
	v_mfma_f32_16x16x32_f16 v[230:233], v[40:43], v[210:213], v[230:233]
	v_mfma_f32_16x16x32_f16 v[222:225], v[40:43], v[218:221], v[222:225]
	v_mfma_f32_16x16x32_f16 v[226:229], v[44:47], v[218:221], v[226:229]
	s_setprio 0
	ds_read_b128 v[44:47], v129 offset:36864
	ds_read_b128 v[48:51], v129 offset:38912
	s_mov_b32 m0, s92
	v_lshl_add_u64 v[40:41], v[92:93], 0, s[58:59]
	global_load_lds_dwordx4 v[40:41], off
	v_cvt_pk_f16_f32 v41, v70, v71
	v_cvt_pk_f16_f32 v40, v68, v69
	ds_write_b64 v100, v[40:41] offset:4096
	s_add_u32 s0, s22, 0x20e00
	s_addc_u32 s1, s90, 0
	global_load_dwordx4 v[40:43], v201, s[0:1] nt
	s_setprio 1
	s_waitcnt lgkmcnt(1)
	v_mfma_f32_16x16x32_f16 v[68:71], v[44:47], v[206:209], v[52:55]
	v_mfma_f32_16x16x32_f16 v[64:67], v[44:47], v[210:213], v[64:67]
	v_mfma_f32_16x16x32_f16 v[120:123], v[44:47], v[218:221], v[120:123]
	v_mfma_f32_16x16x32_f16 v[124:127], v[48:51], v[206:209], v[124:127]
	v_mfma_f32_16x16x32_f16 v[146:149], v[48:51], v[214:217], v[146:149]
	v_mfma_f32_16x16x32_f16 v[134:137], v[48:51], v[218:221], v[134:137]
	v_mfma_f32_16x16x32_f16 v[138:141], v[44:47], v[214:217], v[138:141]
	v_mfma_f32_16x16x32_f16 v[142:145], v[48:51], v[210:213], v[142:145]
	s_setprio 0
	ds_read_b128 v[48:51], v129 offset:40960
	ds_read_b128 v[52:55], v129 offset:43008
	s_mov_b32 m0, s91
	v_lshl_add_u64 v[44:45], v[92:93], 0, s[60:61]
	global_load_lds_dwordx4 v[44:45], off
	v_cvt_pk_f16_f32 v45, v74, v75
	v_cvt_pk_f16_f32 v44, v72, v73
	ds_write_b64 v100, v[44:45] offset:8192
	s_add_u32 s0, s22, 0x40e00
	s_addc_u32 s1, s90, 0
	global_load_dwordx4 v[44:47], v201, s[0:1] nt
	s_setprio 1
	s_waitcnt lgkmcnt(1)
	v_mfma_f32_16x16x32_f16 v[72:75], v[48:51], v[206:209], v[56:59]
	v_mfma_f32_16x16x32_f16 v[242:245], v[48:51], v[210:213], v[246:249]
	v_mfma_f32_16x16x32_f16 v[170:173], v[48:51], v[214:217], v[170:173]
	v_mfma_f32_16x16x32_f16 v[150:153], v[48:51], v[218:221], v[150:153]
	v_mfma_f32_16x16x32_f16 v[162:165], v[52:55], v[206:209], v[162:165]
	v_mfma_f32_16x16x32_f16 v[174:177], v[52:55], v[210:213], v[174:177]
	v_mfma_f32_16x16x32_f16 v[178:181], v[52:55], v[214:217], v[178:181]
	v_mfma_f32_16x16x32_f16 v[154:157], v[52:55], v[218:221], v[154:157]
	s_setprio 0
	ds_read_b128 v[52:55], v129 offset:45056
	ds_read_b128 v[56:59], v129 offset:47104
	s_mov_b32 m0, s73
	v_lshl_add_u64 v[48:49], v[92:93], 0, s[62:63]
	global_load_lds_dwordx4 v[48:49], off
	v_cvt_pk_f16_f32 v49, v78, v79
	v_cvt_pk_f16_f32 v48, v76, v77
	ds_write_b64 v100, v[48:49] offset:12288
	s_add_u32 s0, s22, 0x60e00
	s_addc_u32 s1, s90, 0
	global_load_dwordx4 v[48:51], v201, s[0:1] nt
	s_setprio 1
	s_waitcnt lgkmcnt(1)
	v_mfma_f32_16x16x32_f16 v[76:79], v[52:55], v[206:209], v[60:63]
	v_mfma_f32_16x16x32_f16 v[234:237], v[52:55], v[210:213], v[234:237]
	v_mfma_f32_16x16x32_f16 v[158:161], v[52:55], v[214:217], v[158:161]
	v_mfma_f32_16x16x32_f16 v[166:169], v[52:55], v[218:221], v[166:169]
	v_mfma_f32_16x16x32_f16 v[182:185], v[56:59], v[206:209], v[182:185]
	v_mfma_f32_16x16x32_f16 v[190:193], v[56:59], v[210:213], v[190:193]
	v_mfma_f32_16x16x32_f16 v[202:205], v[56:59], v[214:217], v[202:205]
	v_mfma_f32_16x16x32_f16 v[186:189], v[56:59], v[218:221], v[186:189]
	s_setprio 0
	ds_read_b128 v[206:209], v128 offset:32768
	ds_read_b128 v[210:213], v128 offset:34816
	ds_read_b128 v[214:217], v128 offset:36864
	ds_read_b128 v[218:221], v128 offset:38912
	ds_read_b128 v[56:59], v130 offset:32768
	ds_read_b128 v[60:63], v130 offset:34816
	v_cvt_pk_f16_f32 v53, v82, v83
	v_cvt_pk_f16_f32 v52, v80, v81
	ds_write_b64 v100, v[52:53] offset:16384
	s_add_u32 s0, s22, 0x80e00
	s_addc_u32 s1, s90, 0
	global_load_dwordx4 v[52:55], v201, s[0:1] nt
	s_setprio 1
	s_waitcnt lgkmcnt(1)
	v_mfma_f32_16x16x32_f16 v[80:83], v[56:59], v[206:209], v[238:241]
	v_mfma_f32_16x16x32_f16 v[104:107], v[56:59], v[214:217], v[104:107]
	v_mfma_f32_16x16x32_f16 v[108:111], v[60:63], v[206:209], v[108:111]
	v_mfma_f32_16x16x32_f16 v[112:115], v[60:63], v[210:213], v[112:115]
	v_mfma_f32_16x16x32_f16 v[116:119], v[60:63], v[214:217], v[116:119]
	v_mfma_f32_16x16x32_f16 v[230:233], v[56:59], v[210:213], v[230:233]
	v_mfma_f32_16x16x32_f16 v[222:225], v[56:59], v[218:221], v[222:225]
	v_mfma_f32_16x16x32_f16 v[226:229], v[60:63], v[218:221], v[226:229]
	s_setprio 0
	ds_read_b128 v[60:63], v130 offset:36864
	ds_read_b128 v[238:241], v130 offset:38912
	v_cvt_pk_f16_f32 v57, v86, v87
	v_cvt_pk_f16_f32 v56, v84, v85
	ds_write_b64 v100, v[56:57] offset:20480
	s_add_u32 s0, s22, 0xa0e00
	s_addc_u32 s1, s90, 0
	global_load_dwordx4 v[56:59], v201, s[0:1] nt
	s_setprio 1
	s_waitcnt lgkmcnt(1)
	v_mfma_f32_16x16x32_f16 v[68:71], v[60:63], v[206:209], v[68:71]
	v_mfma_f32_16x16x32_f16 v[64:67], v[60:63], v[210:213], v[64:67]
	v_mfma_f32_16x16x32_f16 v[84:87], v[60:63], v[214:217], v[138:141]
	v_mfma_f32_16x16x32_f16 v[120:123], v[60:63], v[218:221], v[120:123]
	v_mfma_f32_16x16x32_f16 v[124:127], v[238:241], v[206:209], v[124:127]
	v_mfma_f32_16x16x32_f16 v[134:137], v[238:241], v[218:221], v[134:137]
	v_mfma_f32_16x16x32_f16 v[138:141], v[238:241], v[210:213], v[142:145]
	v_mfma_f32_16x16x32_f16 v[142:145], v[238:241], v[214:217], v[146:149]
	s_setprio 0
	s_nop 1
	ds_read_b128 v[146:149], v130 offset:40960
	ds_read_b128 v[238:241], v130 offset:43008
	v_cvt_pk_f16_f32 v61, v90, v91
	v_cvt_pk_f16_f32 v60, v88, v89
	ds_write_b64 v100, v[60:61] offset:24576
	s_add_u32 s0, s22, 0xc0e00
	s_addc_u32 s1, s90, 0
	global_load_dwordx4 v[60:63], v201, s[0:1] nt
	s_setprio 1
	s_waitcnt lgkmcnt(1)
	v_mfma_f32_16x16x32_f16 v[72:75], v[146:149], v[206:209], v[72:75]
	v_mfma_f32_16x16x32_f16 v[88:91], v[146:149], v[210:213], v[242:245]
	v_mfma_f32_16x16x32_f16 v[170:173], v[146:149], v[214:217], v[170:173]
	v_mfma_f32_16x16x32_f16 v[146:149], v[146:149], v[218:221], v[150:153]
	v_mfma_f32_16x16x32_f16 v[150:153], v[238:241], v[206:209], v[162:165]
	v_mfma_f32_16x16x32_f16 v[162:165], v[238:241], v[210:213], v[174:177]
	v_mfma_f32_16x16x32_f16 v[174:177], v[238:241], v[214:217], v[178:181]
	v_mfma_f32_16x16x32_f16 v[154:157], v[238:241], v[218:221], v[154:157]
	s_setprio 0
	s_nop 0
	ds_read_b128 v[178:181], v130 offset:45056
	ds_read_b128 v[238:241], v130 offset:47104
	v_cvt_pk_f16_f32 v39, v38, v39
	v_cvt_pk_f16_f32 v38, v36, v37
	ds_write_b64 v100, v[38:39] offset:28672
	s_add_u32 s0, s22, 0xe0e00
	s_addc_u32 s1, s90, 0
	global_load_dwordx4 v[36:39], v201, s[0:1] nt
	s_setprio 1
	s_waitcnt lgkmcnt(1)
	v_mfma_f32_16x16x32_f16 v[76:79], v[178:181], v[206:209], v[76:79]
	v_mfma_f32_16x16x32_f16 v[234:237], v[178:181], v[210:213], v[234:237]
	v_mfma_f32_16x16x32_f16 v[158:161], v[178:181], v[214:217], v[158:161]
	v_mfma_f32_16x16x32_f16 v[166:169], v[178:181], v[218:221], v[166:169]
	v_mfma_f32_16x16x32_f16 v[178:181], v[238:241], v[206:209], v[182:185]
	v_mfma_f32_16x16x32_f16 v[182:185], v[238:241], v[210:213], v[190:193]
	v_mfma_f32_16x16x32_f16 v[190:193], v[238:241], v[214:217], v[202:205]
	v_mfma_f32_16x16x32_f16 v[186:189], v[238:241], v[218:221], v[186:189]
	s_setprio 0
	s_waitcnt vmcnt(4)
	s_waitcnt lgkmcnt(0)
	s_barrier
	ds_read_b128 v[202:205], v131
	ds_read_b128 v[206:209], v131 offset:2048
	ds_read_b128 v[210:213], v131 offset:4096
	ds_read_b128 v[214:217], v131 offset:6144
	ds_read_b128 v[218:221], v129
	ds_read_b128 v[238:241], v129 offset:2048
	s_add_u32 s70, s22, 0xf00
	v_lshl_add_u64 v[92:93], s[52:53], 0, v[196:197]
	s_addc_u32 s71, s90, 0
	v_readfirstlane_b32 s0, v95
	s_mov_b32 m0, s0
	v_cvt_pk_f16_f32 v3, v2, v3
	global_load_lds_dwordx4 v[92:93], off
	v_cvt_pk_f16_f32 v2, v0, v1
	ds_write_b64 v100, v[2:3] offset:32768
	global_load_dwordx4 v[0:3], v201, s[70:71] nt
	s_setprio 1
	s_waitcnt lgkmcnt(1)
	v_mfma_f32_16x16x32_f16 v[80:83], v[218:221], v[202:205], v[80:83]
	v_mfma_f32_16x16x32_f16 v[104:107], v[218:221], v[210:213], v[104:107]
	v_mfma_f32_16x16x32_f16 v[108:111], v[238:241], v[202:205], v[108:111]
	v_mfma_f32_16x16x32_f16 v[112:115], v[238:241], v[206:209], v[112:115]
	v_mfma_f32_16x16x32_f16 v[116:119], v[238:241], v[210:213], v[116:119]
	v_mfma_f32_16x16x32_f16 v[230:233], v[218:221], v[206:209], v[230:233]
	v_mfma_f32_16x16x32_f16 v[218:221], v[218:221], v[214:217], v[222:225]
	v_mfma_f32_16x16x32_f16 v[222:225], v[238:241], v[214:217], v[226:229]
	s_setprio 0
	s_nop 1
	ds_read_b128 v[226:229], v129 offset:4096
	ds_read_b128 v[238:241], v129 offset:6144
	v_readfirstlane_b32 s1, v96
	v_lshl_add_u64 v[198:199], v[92:93], 0, s[58:59]
	s_mov_b32 m0, s1
	v_cvt_pk_f16_f32 v7, v6, v7
	global_load_lds_dwordx4 v[198:199], off
	v_cvt_pk_f16_f32 v6, v4, v5
	ds_write_b64 v100, v[6:7] offset:36864
	s_add_u32 s70, s22, 0x20f00
	s_addc_u32 s71, s90, 0
	global_load_dwordx4 v[4:7], v201, s[70:71] nt
	s_setprio 1
	s_waitcnt lgkmcnt(1)
	v_mfma_f32_16x16x32_f16 v[68:71], v[226:229], v[202:205], v[68:71]
	v_mfma_f32_16x16x32_f16 v[64:67], v[226:229], v[206:209], v[64:67]
	v_mfma_f32_16x16x32_f16 v[84:87], v[226:229], v[210:213], v[84:87]
	v_mfma_f32_16x16x32_f16 v[120:123], v[226:229], v[214:217], v[120:123]
	v_mfma_f32_16x16x32_f16 v[124:127], v[238:241], v[202:205], v[124:127]
	v_mfma_f32_16x16x32_f16 v[134:137], v[238:241], v[214:217], v[134:137]
	v_mfma_f32_16x16x32_f16 v[138:141], v[238:241], v[206:209], v[138:141]
	v_mfma_f32_16x16x32_f16 v[142:145], v[238:241], v[210:213], v[142:145]
	s_setprio 0
	ds_read_b128 v[226:229], v129 offset:8192
	ds_read_b128 v[238:241], v129 offset:10240
	v_readfirstlane_b32 s70, v97
	v_lshl_add_u64 v[198:199], v[92:93], 0, s[60:61]
	s_mov_b32 m0, s70
	v_cvt_pk_f16_f32 v15, v14, v15
	global_load_lds_dwordx4 v[198:199], off
	v_cvt_pk_f16_f32 v14, v12, v13
	ds_write_b64 v100, v[14:15] offset:40960
	s_add_u32 s72, s22, 0x40f00
	s_addc_u32 s73, s90, 0
	global_load_dwordx4 v[12:15], v201, s[72:73] nt
	s_setprio 1
	s_waitcnt lgkmcnt(1)
	v_mfma_f32_16x16x32_f16 v[72:75], v[226:229], v[202:205], v[72:75]
	v_mfma_f32_16x16x32_f16 v[88:91], v[226:229], v[206:209], v[88:91]
	v_mfma_f32_16x16x32_f16 v[146:149], v[226:229], v[214:217], v[146:149]
	v_mfma_f32_16x16x32_f16 v[170:173], v[226:229], v[210:213], v[170:173]
	v_mfma_f32_16x16x32_f16 v[150:153], v[238:241], v[202:205], v[150:153]
	v_mfma_f32_16x16x32_f16 v[162:165], v[238:241], v[206:209], v[162:165]
	v_mfma_f32_16x16x32_f16 v[174:177], v[238:241], v[210:213], v[174:177]
	v_mfma_f32_16x16x32_f16 v[154:157], v[238:241], v[214:217], v[154:157]
	s_setprio 0
	ds_read_b128 v[226:229], v129 offset:12288
	ds_read_b128 v[238:241], v129 offset:14336
	v_readfirstlane_b32 s71, v98
	v_lshl_add_u64 v[92:93], v[92:93], 0, s[62:63]
	s_mov_b32 m0, s71
	v_cvt_pk_f16_f32 v19, v18, v19
	global_load_lds_dwordx4 v[92:93], off
	v_cvt_pk_f16_f32 v18, v16, v17
	ds_write_b64 v100, v[18:19] offset:45056
	s_add_u32 s72, s22, 0x60f00
	s_addc_u32 s73, s90, 0
	global_load_dwordx4 v[16:19], v201, s[72:73] nt
	s_setprio 1
	s_waitcnt lgkmcnt(1)
	v_mfma_f32_16x16x32_f16 v[76:79], v[226:229], v[202:205], v[76:79]
	v_mfma_f32_16x16x32_f16 v[234:237], v[226:229], v[206:209], v[234:237]
	v_mfma_f32_16x16x32_f16 v[158:161], v[226:229], v[210:213], v[158:161]
	v_mfma_f32_16x16x32_f16 v[166:169], v[226:229], v[214:217], v[166:169]
	v_mfma_f32_16x16x32_f16 v[178:181], v[238:241], v[202:205], v[178:181]
	v_mfma_f32_16x16x32_f16 v[182:185], v[238:241], v[206:209], v[182:185]
	v_mfma_f32_16x16x32_f16 v[190:193], v[238:241], v[210:213], v[190:193]
	v_mfma_f32_16x16x32_f16 v[186:189], v[238:241], v[214:217], v[186:189]
	s_setprio 0
	ds_read_b128 v[202:205], v128
	ds_read_b128 v[206:209], v128 offset:2048
	ds_read_b128 v[210:213], v128 offset:4096
	ds_read_b128 v[214:217], v128 offset:6144
	ds_read_b128 v[226:229], v130
	ds_read_b128 v[238:241], v130 offset:2048
	v_cvt_pk_f16_f32 v23, v22, v23
	v_cvt_pk_f16_f32 v22, v20, v21
	ds_write_b64 v100, v[22:23] offset:49152
	s_add_u32 s72, s22, 0x80f00
	s_addc_u32 s73, s90, 0
	global_load_dwordx4 v[20:23], v201, s[72:73] nt
	s_setprio 1
	s_waitcnt lgkmcnt(1)
	v_mfma_f32_16x16x32_f16 v[80:83], v[226:229], v[202:205], v[80:83]
	v_mfma_f32_16x16x32_f16 v[104:107], v[226:229], v[210:213], v[104:107]
	v_mfma_f32_16x16x32_f16 v[108:111], v[238:241], v[202:205], v[108:111]
	v_mfma_f32_16x16x32_f16 v[112:115], v[238:241], v[206:209], v[112:115]
	v_mfma_f32_16x16x32_f16 v[116:119], v[238:241], v[210:213], v[116:119]
	v_mfma_f32_16x16x32_f16 v[230:233], v[226:229], v[206:209], v[230:233]
	v_mfma_f32_16x16x32_f16 v[218:221], v[226:229], v[214:217], v[218:221]
	v_mfma_f32_16x16x32_f16 v[222:225], v[238:241], v[214:217], v[222:225]
	s_setprio 0
	ds_read_b128 v[226:229], v130 offset:4096
	ds_read_b128 v[238:241], v130 offset:6144
	v_cvt_pk_f16_f32 v27, v26, v27
	v_cvt_pk_f16_f32 v26, v24, v25
	ds_write_b64 v100, v[26:27] offset:53248
	s_add_u32 s72, s22, 0xa0f00
	s_addc_u32 s73, s90, 0
	global_load_dwordx4 v[24:27], v201, s[72:73] nt
	s_setprio 1
	s_waitcnt lgkmcnt(1)
	v_mfma_f32_16x16x32_f16 v[68:71], v[226:229], v[202:205], v[68:71]
	v_mfma_f32_16x16x32_f16 v[64:67], v[226:229], v[206:209], v[64:67]
	v_mfma_f32_16x16x32_f16 v[84:87], v[226:229], v[210:213], v[84:87]
	v_mfma_f32_16x16x32_f16 v[120:123], v[226:229], v[214:217], v[120:123]
	v_mfma_f32_16x16x32_f16 v[124:127], v[238:241], v[202:205], v[124:127]
	v_mfma_f32_16x16x32_f16 v[134:137], v[238:241], v[214:217], v[134:137]
	v_mfma_f32_16x16x32_f16 v[138:141], v[238:241], v[206:209], v[138:141]
	v_mfma_f32_16x16x32_f16 v[142:145], v[238:241], v[210:213], v[142:145]
	s_setprio 0
	ds_read_b128 v[226:229], v130 offset:8192
	ds_read_b128 v[238:241], v130 offset:10240
	v_cvt_pk_f16_f32 v31, v30, v31
	v_cvt_pk_f16_f32 v30, v28, v29
	ds_write_b64 v100, v[30:31] offset:57344
	s_add_u32 s72, s22, 0xc0f00
	s_addc_u32 s73, s90, 0
	global_load_dwordx4 v[28:31], v201, s[72:73] nt
	s_setprio 1
	s_waitcnt lgkmcnt(1)
	v_mfma_f32_16x16x32_f16 v[72:75], v[226:229], v[202:205], v[72:75]
	v_mfma_f32_16x16x32_f16 v[88:91], v[226:229], v[206:209], v[88:91]
	v_mfma_f32_16x16x32_f16 v[146:149], v[226:229], v[214:217], v[146:149]
	v_mfma_f32_16x16x32_f16 v[170:173], v[226:229], v[210:213], v[170:173]
	v_mfma_f32_16x16x32_f16 v[150:153], v[238:241], v[202:205], v[150:153]
	v_mfma_f32_16x16x32_f16 v[162:165], v[238:241], v[206:209], v[162:165]
	v_mfma_f32_16x16x32_f16 v[174:177], v[238:241], v[210:213], v[174:177]
	v_mfma_f32_16x16x32_f16 v[154:157], v[238:241], v[214:217], v[154:157]
	s_setprio 0
	ds_read_b128 v[226:229], v130 offset:12288
	ds_read_b128 v[238:241], v130 offset:14336
	v_cvt_pk_f16_f32 v35, v34, v35
	v_cvt_pk_f16_f32 v34, v32, v33
	ds_write_b64 v100, v[34:35] offset:61440
	s_add_u32 s72, s22, 0xe0f00
	s_addc_u32 s73, s90, 0
	global_load_dwordx4 v[32:35], v201, s[72:73] nt
	s_setprio 1
	s_waitcnt lgkmcnt(1)
	v_mfma_f32_16x16x32_f16 v[76:79], v[226:229], v[202:205], v[76:79]
	v_mfma_f32_16x16x32_f16 v[234:237], v[226:229], v[206:209], v[234:237]
	v_mfma_f32_16x16x32_f16 v[158:161], v[226:229], v[210:213], v[158:161]
	v_mfma_f32_16x16x32_f16 v[166:169], v[226:229], v[214:217], v[166:169]
	v_mfma_f32_16x16x32_f16 v[178:181], v[238:241], v[202:205], v[178:181]
	v_mfma_f32_16x16x32_f16 v[182:185], v[238:241], v[206:209], v[182:185]
	v_mfma_f32_16x16x32_f16 v[190:193], v[238:241], v[210:213], v[190:193]
	v_mfma_f32_16x16x32_f16 v[186:189], v[238:241], v[214:217], v[186:189]
	s_setprio 0
	s_waitcnt vmcnt(4)
	s_waitcnt lgkmcnt(0)
	s_barrier
	ds_read_b128 v[202:205], v131 offset:32768
	ds_read_b128 v[206:209], v131 offset:34816
	ds_read_b128 v[210:213], v131 offset:36864
	ds_read_b128 v[214:217], v131 offset:38912
	ds_read_b128 v[226:229], v129 offset:32768
	ds_read_b128 v[238:241], v129 offset:34816
	v_lshl_add_u64 v[198:199], s[54:55], 0, v[196:197]
	v_readfirstlane_b32 s64, v94
	s_mov_b32 m0, s64
	v_cvt_pk_f16_f32 v11, v10, v11
	global_load_lds_dwordx4 v[198:199], off
	v_cvt_pk_f16_f32 v10, v8, v9
	ds_write_b64 v100, v[10:11]
	s_setprio 1
	s_waitcnt lgkmcnt(1)
	v_mfma_f32_16x16x32_f16 v[8:11], v[226:229], v[202:205], v[80:83]
	v_mfma_f32_16x16x32_f16 v[80:83], v[226:229], v[206:209], v[230:233]
	v_mfma_f32_16x16x32_f16 v[92:95], v[226:229], v[210:213], v[104:107]
	v_mfma_f32_16x16x32_f16 v[104:107], v[226:229], v[214:217], v[218:221]
	v_mfma_f32_16x16x32_f16 v[108:111], v[238:241], v[202:205], v[108:111]
	v_mfma_f32_16x16x32_f16 v[112:115], v[238:241], v[206:209], v[112:115]
	v_mfma_f32_16x16x32_f16 v[116:119], v[238:241], v[210:213], v[116:119]
	v_mfma_f32_16x16x32_f16 v[218:221], v[238:241], v[214:217], v[222:225]
	s_setprio 0
	s_nop 1
	ds_read_b128 v[222:225], v129 offset:36864
	ds_read_b128 v[226:229], v129 offset:38912
	v_readfirstlane_b32 s64, v99
	v_lshl_add_u64 v[96:97], v[198:199], 0, s[58:59]
	s_mov_b32 m0, s64
	v_cvt_pk_f16_f32 v43, v42, v43
	global_load_lds_dwordx4 v[96:97], off
	v_cvt_pk_f16_f32 v42, v40, v41
	ds_write_b64 v100, v[42:43] offset:4096
	s_setprio 1
	s_waitcnt lgkmcnt(1)
	v_mfma_f32_16x16x32_f16 v[40:43], v[222:225], v[202:205], v[68:71]
	v_mfma_f32_16x16x32_f16 v[64:67], v[222:225], v[206:209], v[64:67]
	v_mfma_f32_16x16x32_f16 v[68:71], v[222:225], v[210:213], v[84:87]
	v_mfma_f32_16x16x32_f16 v[84:87], v[222:225], v[214:217], v[120:123]
	v_mfma_f32_16x16x32_f16 v[96:99], v[226:229], v[202:205], v[124:127]
	v_mfma_f32_16x16x32_f16 v[120:123], v[226:229], v[206:209], v[138:141]
	v_mfma_f32_16x16x32_f16 v[124:127], v[226:229], v[210:213], v[142:145]
	v_mfma_f32_16x16x32_f16 v[134:137], v[226:229], v[214:217], v[134:137]
	s_setprio 0
	ds_read_b128 v[138:141], v129 offset:40960
	ds_read_b128 v[142:145], v129 offset:43008
	v_readfirstlane_b32 s64, v101
	v_lshl_add_u64 v[222:223], v[198:199], 0, s[60:61]
	s_mov_b32 m0, s64
	v_cvt_pk_f16_f32 v47, v46, v47
	global_load_lds_dwordx4 v[222:223], off
	v_cvt_pk_f16_f32 v46, v44, v45
	ds_write_b64 v100, v[46:47] offset:8192
	s_setprio 1
	s_waitcnt lgkmcnt(1)
	v_mfma_f32_16x16x32_f16 v[44:47], v[138:141], v[202:205], v[72:75]
	v_mfma_f32_16x16x32_f16 v[72:75], v[138:141], v[206:209], v[88:91]
	v_mfma_f32_16x16x32_f16 v[88:91], v[138:141], v[210:213], v[170:173]
	v_mfma_f32_16x16x32_f16 v[138:141], v[138:141], v[214:217], v[146:149]
	v_mfma_f32_16x16x32_f16 v[146:149], v[142:145], v[202:205], v[150:153]
	v_mfma_f32_16x16x32_f16 v[150:153], v[142:145], v[206:209], v[162:165]
	v_mfma_f32_16x16x32_f16 v[162:165], v[142:145], v[210:213], v[174:177]
	v_mfma_f32_16x16x32_f16 v[142:145], v[142:145], v[214:217], v[154:157]
	s_setprio 0
	s_nop 1
	ds_read_b128 v[154:157], v129 offset:45056
	ds_read_b128 v[170:173], v129 offset:47104
	v_readfirstlane_b32 s64, v102
	v_lshl_add_u64 v[174:175], v[198:199], 0, s[62:63]
	s_mov_b32 m0, s64
	v_cvt_pk_f16_f32 v51, v50, v51
	global_load_lds_dwordx4 v[174:175], off
	v_cvt_pk_f16_f32 v50, v48, v49
	ds_write_b64 v100, v[50:51] offset:12288
	s_setprio 1
	s_waitcnt lgkmcnt(1)
	v_mfma_f32_16x16x32_f16 v[48:51], v[154:157], v[202:205], v[76:79]
	v_mfma_f32_16x16x32_f16 v[76:79], v[154:157], v[206:209], v[234:237]
	v_mfma_f32_16x16x32_f16 v[158:161], v[154:157], v[210:213], v[158:161]
	v_mfma_f32_16x16x32_f16 v[154:157], v[154:157], v[214:217], v[166:169]
	v_mfma_f32_16x16x32_f16 v[166:169], v[170:173], v[202:205], v[178:181]
	v_mfma_f32_16x16x32_f16 v[174:177], v[170:173], v[206:209], v[182:185]
	v_mfma_f32_16x16x32_f16 v[178:181], v[170:173], v[210:213], v[190:193]
	v_mfma_f32_16x16x32_f16 v[170:173], v[170:173], v[214:217], v[186:189]
	s_setprio 0
	ds_read_b128 v[182:185], v128 offset:32768
	s_nop 0
	ds_read_b128 v[186:189], v128 offset:34816
	ds_read_b128 v[190:193], v128 offset:36864
	ds_read_b128 v[202:205], v128 offset:38912
	ds_read_b128 v[206:209], v130 offset:32768
	ds_read_b128 v[210:213], v130 offset:34816
	v_cvt_pk_f16_f32 v55, v54, v55
	v_cvt_pk_f16_f32 v54, v52, v53
	ds_write_b64 v100, v[54:55] offset:16384
	s_setprio 1
	s_waitcnt lgkmcnt(1)
	v_mfma_f32_16x16x32_f16 v[8:11], v[206:209], v[182:185], v[8:11]
	v_mfma_f32_16x16x32_f16 v[52:55], v[206:209], v[186:189], v[80:83]
	v_mfma_f32_16x16x32_f16 v[80:83], v[206:209], v[190:193], v[92:95]
	v_mfma_f32_16x16x32_f16 v[92:95], v[206:209], v[202:205], v[104:107]
	v_mfma_f32_16x16x32_f16 v[102:105], v[210:213], v[182:185], v[108:111]
	v_mfma_f32_16x16x32_f16 v[106:109], v[210:213], v[186:189], v[112:115]
	v_mfma_f32_16x16x32_f16 v[110:113], v[210:213], v[190:193], v[116:119]
	v_mfma_f32_16x16x32_f16 v[114:117], v[210:213], v[202:205], v[218:221]
	s_setprio 0
	ds_read_b128 v[206:209], v130 offset:36864
	ds_read_b128 v[210:213], v130 offset:38912
	v_cvt_pk_f16_f32 v59, v58, v59
	v_cvt_pk_f16_f32 v58, v56, v57
	ds_write_b64 v100, v[58:59] offset:20480
	s_setprio 1
	s_waitcnt lgkmcnt(1)
	v_mfma_f32_16x16x32_f16 v[40:43], v[206:209], v[182:185], v[40:43]
	v_mfma_f32_16x16x32_f16 v[56:59], v[206:209], v[186:189], v[64:67]
	v_mfma_f32_16x16x32_f16 v[64:67], v[206:209], v[190:193], v[68:71]
	v_mfma_f32_16x16x32_f16 v[68:71], v[206:209], v[202:205], v[84:87]
	v_mfma_f32_16x16x32_f16 v[84:87], v[210:213], v[182:185], v[96:99]
	v_mfma_f32_16x16x32_f16 v[96:99], v[210:213], v[186:189], v[120:123]
	v_mfma_f32_16x16x32_f16 v[118:121], v[210:213], v[190:193], v[124:127]
	v_mfma_f32_16x16x32_f16 v[122:125], v[210:213], v[202:205], v[134:137]
	s_setprio 0
	s_nop 1
	ds_read_b128 v[134:137], v130 offset:40960
	ds_read_b128 v[206:209], v130 offset:43008
	v_cvt_pk_f16_f32 v63, v62, v63
	v_cvt_pk_f16_f32 v62, v60, v61
	ds_write_b64 v100, v[62:63] offset:24576
	s_setprio 1
	s_waitcnt lgkmcnt(1)
	v_mfma_f32_16x16x32_f16 v[44:47], v[134:137], v[182:185], v[44:47]
	v_mfma_f32_16x16x32_f16 v[60:63], v[134:137], v[186:189], v[72:75]
	v_mfma_f32_16x16x32_f16 v[72:75], v[134:137], v[190:193], v[88:91]
	v_mfma_f32_16x16x32_f16 v[88:91], v[134:137], v[202:205], v[138:141]
	v_mfma_f32_16x16x32_f16 v[134:137], v[206:209], v[182:185], v[146:149]
	v_mfma_f32_16x16x32_f16 v[146:149], v[206:209], v[190:193], v[162:165]
	v_mfma_f32_16x16x32_f16 v[138:141], v[206:209], v[186:189], v[150:153]
	v_mfma_f32_16x16x32_f16 v[142:145], v[206:209], v[202:205], v[142:145]
	s_setprio 0
	s_nop 0
	ds_read_b128 v[150:153], v130 offset:45056
	ds_read_b128 v[162:165], v130 offset:47104
	v_cvt_pk_f16_f32 v39, v38, v39
	v_cvt_pk_f16_f32 v38, v36, v37
	ds_write_b64 v100, v[38:39] offset:28672
	s_setprio 1
	s_waitcnt lgkmcnt(1)
	v_mfma_f32_16x16x32_f16 v[36:39], v[150:153], v[182:185], v[48:51]
	v_mfma_f32_16x16x32_f16 v[48:51], v[150:153], v[186:189], v[76:79]
	v_mfma_f32_16x16x32_f16 v[76:79], v[150:153], v[190:193], v[158:161]
	v_mfma_f32_16x16x32_f16 v[150:153], v[150:153], v[202:205], v[154:157]
	v_mfma_f32_16x16x32_f16 v[154:157], v[162:165], v[182:185], v[166:169]
	v_mfma_f32_16x16x32_f16 v[158:161], v[162:165], v[186:189], v[174:177]
	v_mfma_f32_16x16x32_f16 v[166:169], v[162:165], v[190:193], v[178:181]
	v_mfma_f32_16x16x32_f16 v[162:165], v[162:165], v[202:205], v[170:173]
	s_setprio 0
	s_waitcnt vmcnt(0)
	s_waitcnt lgkmcnt(0)
	s_barrier
	s_nop 0
	ds_read_b128 v[170:173], v131
	ds_read_b128 v[174:177], v131 offset:2048
	ds_read_b128 v[178:181], v131 offset:4096
	ds_read_b128 v[182:185], v131 offset:6144
	ds_read_b128 v[186:189], v129
	ds_read_b128 v[190:193], v129 offset:2048
	v_lshl_add_u64 v[126:127], s[56:57], 0, v[196:197]
	s_mov_b32 m0, s0
	v_cvt_pk_f16_f32 v3, v2, v3
	global_load_lds_dwordx4 v[126:127], off
	v_cvt_pk_f16_f32 v2, v0, v1
	ds_write_b64 v100, v[2:3] offset:32768
	s_setprio 1
	s_waitcnt lgkmcnt(1)
	v_mfma_f32_16x16x32_f16 v[0:3], v[186:189], v[170:173], v[8:11]
	v_mfma_f32_16x16x32_f16 v[8:11], v[186:189], v[174:177], v[52:55]
	v_mfma_f32_16x16x32_f16 v[52:55], v[186:189], v[178:181], v[80:83]
	v_mfma_f32_16x16x32_f16 v[80:83], v[186:189], v[182:185], v[92:95]
	v_mfma_f32_16x16x32_f16 v[92:95], v[190:193], v[170:173], v[102:105]
	v_mfma_f32_16x16x32_f16 v[102:105], v[190:193], v[174:177], v[106:109]
	v_mfma_f32_16x16x32_f16 v[106:109], v[190:193], v[178:181], v[110:113]
	v_mfma_f32_16x16x32_f16 v[110:113], v[190:193], v[182:185], v[114:117]
	s_setprio 0
	s_nop 1
	ds_read_b128 v[114:117], v129 offset:4096
	ds_read_b128 v[186:189], v129 offset:6144
	s_mov_b32 m0, s1
	v_lshl_add_u64 v[190:191], v[126:127], 0, s[58:59]
	global_load_lds_dwordx4 v[190:191], off
	v_cvt_pk_f16_f32 v7, v6, v7
	v_cvt_pk_f16_f32 v6, v4, v5
	ds_write_b64 v100, v[6:7] offset:36864
	s_setprio 1
	s_waitcnt lgkmcnt(1)
	v_mfma_f32_16x16x32_f16 v[190:193], v[114:117], v[170:173], v[40:43]
	v_mfma_f32_16x16x32_f16 v[56:59], v[114:117], v[174:177], v[56:59]
	v_mfma_f32_16x16x32_f16 v[64:67], v[114:117], v[178:181], v[64:67]
	v_mfma_f32_16x16x32_f16 v[68:71], v[114:117], v[182:185], v[68:71]
	v_mfma_f32_16x16x32_f16 v[84:87], v[186:189], v[170:173], v[84:87]
	v_mfma_f32_16x16x32_f16 v[96:99], v[186:189], v[174:177], v[96:99]
	v_mfma_f32_16x16x32_f16 v[114:117], v[186:189], v[178:181], v[118:121]
	v_mfma_f32_16x16x32_f16 v[118:121], v[186:189], v[182:185], v[122:125]
	s_setprio 0
	ds_read_b128 v[4:7], v129 offset:8192
	ds_read_b128 v[40:43], v129 offset:10240
	s_mov_b32 m0, s70
	v_lshl_add_u64 v[122:123], v[126:127], 0, s[60:61]
	global_load_lds_dwordx4 v[122:123], off
	v_cvt_pk_f16_f32 v15, v14, v15
	v_cvt_pk_f16_f32 v14, v12, v13
	ds_write_b64 v100, v[14:15] offset:40960
	s_setprio 1
	s_waitcnt lgkmcnt(1)
	v_mfma_f32_16x16x32_f16 v[122:125], v[4:7], v[170:173], v[44:47]
	v_mfma_f32_16x16x32_f16 v[88:91], v[4:7], v[182:185], v[88:91]
	v_mfma_f32_16x16x32_f16 v[134:137], v[40:43], v[170:173], v[134:137]
	v_mfma_f32_16x16x32_f16 v[146:149], v[40:43], v[178:181], v[146:149]
	v_mfma_f32_16x16x32_f16 v[186:189], v[4:7], v[174:177], v[60:63]
	v_mfma_f32_16x16x32_f16 v[202:205], v[4:7], v[178:181], v[72:75]
	v_mfma_f32_16x16x32_f16 v[138:141], v[40:43], v[174:177], v[138:141]
	v_mfma_f32_16x16x32_f16 v[142:145], v[40:43], v[182:185], v[142:145]
	s_setprio 0
	ds_read_b128 v[4:7], v129 offset:12288
	ds_read_b128 v[12:15], v129 offset:14336
	s_mov_b32 m0, s71
	v_lshl_add_u64 v[40:41], v[126:127], 0, s[62:63]
	global_load_lds_dwordx4 v[40:41], off
	v_cvt_pk_f16_f32 v19, v18, v19
	v_cvt_pk_f16_f32 v18, v16, v17
	ds_write_b64 v100, v[18:19] offset:45056
	s_setprio 1
	s_waitcnt lgkmcnt(1)
	v_mfma_f32_16x16x32_f16 v[206:209], v[4:7], v[170:173], v[36:39]
	v_mfma_f32_16x16x32_f16 v[210:213], v[4:7], v[174:177], v[48:51]
	v_mfma_f32_16x16x32_f16 v[214:217], v[4:7], v[178:181], v[76:79]
	v_mfma_f32_16x16x32_f16 v[150:153], v[4:7], v[182:185], v[150:153]
	v_mfma_f32_16x16x32_f16 v[154:157], v[12:15], v[170:173], v[154:157]
	v_mfma_f32_16x16x32_f16 v[158:161], v[12:15], v[174:177], v[158:161]
	v_mfma_f32_16x16x32_f16 v[166:169], v[12:15], v[178:181], v[166:169]
	v_mfma_f32_16x16x32_f16 v[162:165], v[12:15], v[182:185], v[162:165]
	s_setprio 0
	ds_read_b128 v[170:173], v128
	ds_read_b128 v[174:177], v128 offset:2048
	ds_read_b128 v[178:181], v128 offset:4096
	ds_read_b128 v[182:185], v128 offset:6144
	ds_read_b128 v[12:15], v130
	ds_read_b128 v[40:43], v130 offset:2048
	v_cvt_pk_f16_f32 v5, v22, v23
	v_cvt_pk_f16_f32 v4, v20, v21
	ds_write_b64 v100, v[4:5] offset:49152
	s_setprio 1
	s_waitcnt lgkmcnt(1)
	v_mfma_f32_16x16x32_f16 v[0:3], v[12:15], v[170:173], v[0:3]
	v_mfma_f32_16x16x32_f16 v[4:7], v[12:15], v[174:177], v[8:11]
	v_mfma_f32_16x16x32_f16 v[8:11], v[12:15], v[178:181], v[52:55]
	v_mfma_f32_16x16x32_f16 v[12:15], v[12:15], v[182:185], v[80:83]
	v_mfma_f32_16x16x32_f16 v[16:19], v[40:43], v[170:173], v[92:95]
	v_mfma_f32_16x16x32_f16 v[20:23], v[40:43], v[174:177], v[102:105]
	v_mfma_f32_16x16x32_f16 v[36:39], v[40:43], v[178:181], v[106:109]
	v_mfma_f32_16x16x32_f16 v[40:43], v[40:43], v[182:185], v[110:113]
	s_setprio 0
	ds_read_b128 v[52:55], v130 offset:4096
	ds_read_b128 v[72:75], v130 offset:6144
	v_cvt_pk_f16_f32 v27, v26, v27
	v_cvt_pk_f16_f32 v26, v24, v25
	ds_write_b64 v100, v[26:27] offset:53248
	s_setprio 1
	s_waitcnt lgkmcnt(1)
	v_mfma_f32_16x16x32_f16 v[24:27], v[52:55], v[170:173], v[190:193]
	v_mfma_f32_16x16x32_f16 v[44:47], v[52:55], v[174:177], v[56:59]
	v_mfma_f32_16x16x32_f16 v[48:51], v[52:55], v[178:181], v[64:67]
	v_mfma_f32_16x16x32_f16 v[52:55], v[52:55], v[182:185], v[68:71]
	v_mfma_f32_16x16x32_f16 v[56:59], v[72:75], v[170:173], v[84:87]
	v_mfma_f32_16x16x32_f16 v[60:63], v[72:75], v[174:177], v[96:99]
	v_mfma_f32_16x16x32_f16 v[64:67], v[72:75], v[178:181], v[114:117]
	v_mfma_f32_16x16x32_f16 v[68:71], v[72:75], v[182:185], v[118:121]
	s_setprio 0
	ds_read_b128 v[80:83], v130 offset:8192
	ds_read_b128 v[96:99], v130 offset:10240
	v_cvt_pk_f16_f32 v31, v30, v31
	v_cvt_pk_f16_f32 v30, v28, v29
	ds_write_b64 v100, v[30:31] offset:57344
	s_setprio 1
	s_waitcnt lgkmcnt(1)
	v_mfma_f32_16x16x32_f16 v[28:31], v[80:83], v[170:173], v[122:125]
	v_mfma_f32_16x16x32_f16 v[72:75], v[80:83], v[174:177], v[186:189]
	v_mfma_f32_16x16x32_f16 v[76:79], v[80:83], v[178:181], v[202:205]
	v_mfma_f32_16x16x32_f16 v[80:83], v[80:83], v[182:185], v[88:91]
	v_mfma_f32_16x16x32_f16 v[84:87], v[96:99], v[170:173], v[134:137]
	v_mfma_f32_16x16x32_f16 v[88:91], v[96:99], v[174:177], v[138:141]
	v_mfma_f32_16x16x32_f16 v[92:95], v[96:99], v[178:181], v[146:149]
	v_mfma_f32_16x16x32_f16 v[96:99], v[96:99], v[182:185], v[142:145]
	s_setprio 0
	ds_read_b128 v[108:111], v130 offset:12288
	ds_read_b128 v[124:127], v130 offset:14336
	v_cvt_pk_f16_f32 v35, v34, v35
	v_cvt_pk_f16_f32 v34, v32, v33
	ds_write_b64 v100, v[34:35] offset:61440
	s_setprio 1
	s_waitcnt lgkmcnt(1)
	v_mfma_f32_16x16x32_f16 v[32:35], v[108:111], v[170:173], v[206:209]
	v_mfma_f32_16x16x32_f16 v[100:103], v[108:111], v[174:177], v[210:213]
	v_mfma_f32_16x16x32_f16 v[104:107], v[108:111], v[178:181], v[214:217]
	v_mfma_f32_16x16x32_f16 v[108:111], v[108:111], v[182:185], v[150:153]
	v_mfma_f32_16x16x32_f16 v[112:115], v[124:127], v[170:173], v[154:157]
	v_mfma_f32_16x16x32_f16 v[116:119], v[124:127], v[174:177], v[158:161]
	v_mfma_f32_16x16x32_f16 v[120:123], v[124:127], v[178:181], v[166:169]
	v_mfma_f32_16x16x32_f16 v[124:127], v[124:127], v[182:185], v[162:165]
	s_setprio 0
	s_waitcnt vmcnt(0)
	s_waitcnt lgkmcnt(0)
	s_barrier
	ds_read_b128 v[134:137], v131 offset:32768
	ds_read_b128 v[138:141], v131 offset:34816
	ds_read_b128 v[142:145], v131 offset:36864
	ds_read_b128 v[148:151], v131 offset:38912
	ds_read_b128 v[152:155], v129 offset:32768
	ds_read_b128 v[156:159], v129 offset:34816
	s_setprio 1
	s_waitcnt lgkmcnt(0)
	v_mfma_f32_16x16x32_f16 v[0:3], v[152:155], v[134:137], v[0:3]
	v_mfma_f32_16x16x32_f16 v[4:7], v[152:155], v[138:141], v[4:7]
	v_mfma_f32_16x16x32_f16 v[8:11], v[152:155], v[142:145], v[8:11]
	v_mfma_f32_16x16x32_f16 v[12:15], v[152:155], v[148:151], v[12:15]
	v_mfma_f32_16x16x32_f16 v[16:19], v[156:159], v[134:137], v[16:19]
	v_mfma_f32_16x16x32_f16 v[20:23], v[156:159], v[138:141], v[20:23]
	v_mfma_f32_16x16x32_f16 v[36:39], v[156:159], v[142:145], v[36:39]
	v_mfma_f32_16x16x32_f16 v[40:43], v[156:159], v[148:151], v[40:43]
	s_setprio 0
	ds_read_b128 v[152:155], v129 offset:36864
	ds_read_b128 v[156:159], v129 offset:38912
	v_and_b32_e32 v250, 0x7ffffc00, v194
	v_lshl_add_u64 v[252:253], s[10:11], 0, v[196:197]
	v_readfirstlane_b32 s32, v250
	s_nop 0
	s_mov_b32 m0, s32
	s_nop 0
	global_load_lds_dwordx4 v[252:253], off
	v_mov_b32_e32 v146, 0
	v_and_b32_e32 v251, 0xfffffff, v132
	v_cmp_gt_u32_e32 vcc, s82, v251
	v_mov_b32_e32 v132, 0
	v_mov_b32_e32 v133, 0
	s_and_saveexec_b64 s[0:1], vcc
	s_cbranch_execz .LBB1_7
	s_and_b32 s64, s78, 0x7ffffc00
	s_or_b32 s64, s64, s33
	v_or_b32_e32 v132, s64, v251
	v_mov_b32_e32 v133, v195
	v_lshl_add_u64 v[132:133], v[132:133], 2, s[12:13]
	global_load_dword v133, v[132:133], off
	v_or_b32_e32 v132, s33, v251
	v_lshlrev_b32_e32 v132, 2, v132
	global_load_dword v146, v132, s[16:17]
	s_nop 0
	global_load_dword v132, v132, s[14:15]
